# router K-loop staged through LDS: full-line DMA pieces (8 rows x 128 B) shared by all 8 waves, 3-buffer ring, wave=(token group, k-step)
# speedup vs baseline: 1.0755x; 1.0220x over previous
; __device__ __forceinline__ void p5_router(Frame& F) {
;     ...
;     for (int tile = F.bid; tile < M / 64; tile += F.G) {
;         const int m0 = tile * 64;
;         { const int tg = wave & 1, kq = wave >> 1, fr = lane & 15, fq = lane >> 4;
;           f32x4 acc[2][5];
; #pragma unroll
;           for (int a = 0; a < 2; ++a)
; #pragma unroll
;               for (int n = 0; n < 5; ++n) acc[a][n] = (f32x4){0.f, 0.f, 0.f, 0.f};
;           float ss[2] = {0.f, 0.f};
;           const size_t roff = (size_t)(m0 + 32 * tg + fr) * D + kq * 1024 + 8 * fq;
;           const bf16_t* h0 = H + roff; const bf16_t* h1 = h0 + (size_t)16 * D;
;           const float* gp = F.g_ffn + kq * 1024 + 8 * fq;
;           const bf16_t* bh = RBH + (size_t)fr * D + kq * 1024 + 8 * fq; const bf16_t* bl = RBL + (size_t)fr * D + kq * 1024 + 8 * fq;
;           RtLoad La, Lb; rt_load(La, h0, h1, gp, 0);
.LBB0_606:
	s_lshl_b32 s10, s64, 6
	v_readlane_b32 s84, v254, 23
	v_readlane_b32 s86, v254, 31
	v_readlane_b32 s87, v254, 32
	v_readlane_b32 s66, v254, 9
	v_readlane_b32 s67, v254, 10
	s_and_b32 s88, s84, 3
	s_lshr_b32 s89, s84, 2
	s_mov_b32 s94, 0xe00000
	s_mov_b32 s95, 0xea0000
	s_lshl_b32 s91, s64, 19
	s_add_i32 s91, s91, 0x29e00000
	v_and_b32_e32 v217, 7, v131
	v_lshrrev_b32_e32 v218, 1, v130
	v_lshlrev_b32_e32 v219, 13, v130
	s_add_i32 s24, s84, 0
	s_lshl_b32 s98, s24, 10
	s_sub_i32 s85, s24, 10
	s_sub_i32 s33, s24, 20
	s_cmp_lt_u32 s24, 20
	s_cselect_b32 s33, s85, s33
	s_cselect_b32 s85, s95, s91
	s_cmp_lt_u32 s24, 10
	s_cselect_b32 s33, s24, s33
	s_cselect_b32 s85, s94, s85
	s_and_b32 s24, s33, 1
	s_lshl_b32 s24, s24, 2
	s_lshl_b32 s33, s33, 16
	s_add_i32 s85, s85, s33
	v_add_u32_e32 v220, s24, v218
	v_xor_b32_e32 v220, v220, v217
	v_lshl_add_u32 v220, v220, 4, v219
	v_add_u32_e32 v208, s85, v220
	s_add_i32 s24, s84, 8
	s_lshl_b32 s99, s24, 10
	s_sub_i32 s85, s24, 10
	s_sub_i32 s33, s24, 20
	s_cmp_lt_u32 s24, 20
	s_cselect_b32 s33, s85, s33
	s_cselect_b32 s85, s95, s91
	s_cmp_lt_u32 s24, 10
	s_cselect_b32 s33, s24, s33
	s_cselect_b32 s85, s94, s85
	s_and_b32 s24, s33, 1
	s_lshl_b32 s24, s24, 2
	s_lshl_b32 s33, s33, 16
	s_add_i32 s85, s85, s33
	v_add_u32_e32 v220, s24, v218
	v_xor_b32_e32 v220, v220, v217
	v_lshl_add_u32 v220, v220, 4, v219
	v_add_u32_e32 v209, s85, v220
	s_add_i32 s24, s84, 16
	s_lshl_b32 s100, s24, 10
	s_sub_i32 s85, s24, 10
	s_sub_i32 s33, s24, 20
	s_cmp_lt_u32 s24, 20
	s_cselect_b32 s33, s85, s33
	s_cselect_b32 s85, s95, s91
	s_cmp_lt_u32 s24, 10
	s_cselect_b32 s33, s24, s33
	s_cselect_b32 s85, s94, s85
	s_and_b32 s24, s33, 1
	s_lshl_b32 s24, s24, 2
	s_lshl_b32 s33, s33, 16
	s_add_i32 s85, s85, s33
	v_add_u32_e32 v220, s24, v218
	v_xor_b32_e32 v220, v220, v217
	v_lshl_add_u32 v220, v220, 4, v219
	v_add_u32_e32 v210, s85, v220
	s_add_i32 s24, s84, 24
	s_lshl_b32 s101, s24, 10
	s_sub_i32 s85, s24, 10
	s_sub_i32 s33, s24, 20
	s_cmp_lt_u32 s24, 20
	s_cselect_b32 s33, s85, s33
	s_cselect_b32 s85, s95, s91
	s_cmp_lt_u32 s24, 10
	s_cselect_b32 s33, s24, s33
	s_cselect_b32 s85, s94, s85
	s_and_b32 s24, s33, 1
	s_lshl_b32 s24, s24, 2
	s_lshl_b32 s33, s33, 16
	s_add_i32 s85, s85, s33
	v_add_u32_e32 v220, s24, v218
	v_xor_b32_e32 v220, v220, v217
	v_lshl_add_u32 v220, v220, 4, v219
	v_add_u32_e32 v211, s85, v220
	s_lshl_b32 s24, s89, 2
	v_add_u32_e32 v217, s24, v171
	v_bfe_u32 v218, v131, 1, 3
	v_xor_b32_e32 v217, v217, v218
	v_lshlrev_b32_e32 v217, 4, v217
	v_lshl_add_u32 v212, v170, 7, v217
	s_lshl_b32 s24, s88, 11
	s_add_i32 s24, s24, 20480
	v_add_u32_e32 v213, s24, v212
	s_lshl_b32 s24, s89, 7
	v_lshl_add_u32 v216, v171, 5, s24
	global_load_dwordx4 v[42:45], v216, s[66:67]
	global_load_dwordx4 v[46:49], v216, s[66:67] offset:16
	s_mov_b32 m0, s98
	s_nop 0
	global_load_lds_dwordx4 v208, s[86:87]
	s_add_i32 m0, s98, 28672
	v_add_u32_e32 v208, 0x80, v208
	global_load_lds_dwordx4 v208, s[86:87]
	s_mov_b32 m0, s99
	s_nop 0
	global_load_lds_dwordx4 v209, s[86:87]
	s_add_i32 m0, s99, 28672
	v_add_u32_e32 v209, 0x80, v209
	global_load_lds_dwordx4 v209, s[86:87]
	s_mov_b32 m0, s100
	s_nop 0
	global_load_lds_dwordx4 v210, s[86:87]
	s_add_i32 m0, s100, 28672
	v_add_u32_e32 v210, 0x80, v210
	global_load_lds_dwordx4 v210, s[86:87]
	s_cmp_gt_u32 s84, 3
	s_cbranch_scc1 .Lrt_no4
	s_mov_b32 m0, s101
	s_nop 0
	global_load_lds_dwordx4 v211, s[86:87]
	s_add_i32 m0, s101, 28672
	v_add_u32_e32 v211, 0x80, v211
	global_load_lds_dwordx4 v211, s[86:87]
.Lrt_no4:
	v_mov_b32_e32 v18, 0
	v_mov_b32_e32 v19, 0
	v_mov_b32_e32 v20, 0
	v_mov_b32_e32 v21, 0
	v_mov_b32_e32 v22, 0
	v_mov_b32_e32 v23, 0
	v_mov_b32_e32 v24, 0
	v_mov_b32_e32 v25, 0
	v_mov_b32_e32 v26, 0
	v_mov_b32_e32 v27, 0
	v_mov_b32_e32 v28, 0
	v_mov_b32_e32 v29, 0
	v_mov_b32_e32 v30, 0
	v_mov_b32_e32 v31, 0
	v_mov_b32_e32 v32, 0
	v_mov_b32_e32 v33, 0
	v_mov_b32_e32 v34, 0
	v_mov_b32_e32 v35, 0
	v_mov_b32_e32 v36, 0
	v_mov_b32_e32 v37, 0
	v_mov_b32_e32 v224, 0
	s_mov_b32 s94, 0
	s_mov_b32 s95, 28672
	s_mov_b32 s91, 57344
	s_waitcnt vmcnt(0)
	s_barrier
	s_cmp_gt_u32 s84, 3
	s_cbranch_scc1 .Lrt_path3
	v_add_u32_e32 v216, 0x100, v216
	global_load_dwordx4 v[50:53], v216, s[66:67]
	global_load_dwordx4 v[54:57], v216, s[66:67] offset:16
	s_add_i32 m0, s91, s98
	v_add_u32_e32 v208, 0x80, v208
	global_load_lds_dwordx4 v208, s[86:87]
	s_add_i32 m0, s91, s99
	v_add_u32_e32 v209, 0x80, v209
	global_load_lds_dwordx4 v209, s[86:87]
	s_add_i32 m0, s91, s100
	v_add_u32_e32 v210, 0x80, v210
	global_load_lds_dwordx4 v210, s[86:87]
	s_add_i32 m0, s91, s101
	v_add_u32_e32 v211, 0x80, v211
	global_load_lds_dwordx4 v211, s[86:87]
	v_add_u32_e32 v214, s94, v212
	v_add_u32_e32 v215, s94, v213
	ds_read_b128 v[38:41], v215
	ds_read_b128 v[58:61], v214 offset:0
	ds_read_b128 v[62:65], v214 offset:2048
	ds_read_b128 v[66:69], v214 offset:4096
	ds_read_b128 v[70:73], v214 offset:6144
	ds_read_b128 v[74:77], v214 offset:8192
	ds_read_b128 v[100:103], v214 offset:10240
	ds_read_b128 v[104:107], v214 offset:12288
	ds_read_b128 v[108:111], v214 offset:14336
	ds_read_b128 v[112:115], v214 offset:16384
	ds_read_b128 v[116:119], v214 offset:18432
	s_waitcnt lgkmcnt(10)
; __device__ __forceinline__ unsigned f2bf(float f) { unsigned u = __builtin_bit_cast(unsigned, f); return (u + 0x7fffu + ((u >> 16) & 1u)) >> 16; }
; __device__ __forceinline__ void rt_step(const RtLoad& L, const bf16_t* bh, const bf16_t* bl, f32x4 (&acc)[2][5], float (&ss)[2], int ko) {
;     RtW W;
; #pragma unroll
;     for (int n = 0; n < 5; ++n) { W.wh[n] = *(const bf16x8*)(bh + (size_t)n * 16 * D + ko); W.wl[n] = *(const bf16x8*)(bl + (size_t)n * 16 * D + ko); }
;     bf16x8 ahi[2], alo[2];
; #pragma unroll
;     for (int mi = 0; mi < 2; ++mi) { const u32x4 xw = L.x[mi]; const f32x4 xa = (f32x4){bflo(xw.x), bfhi(xw.x), bflo(xw.y), bfhi(xw.y)}, xb = (f32x4){bflo(xw.z), bfhi(xw.z), bflo(xw.w), bfhi(xw.w)};
;         ss[mi] += (xa.x * xa.x + xa.y * xa.y) + (xa.z * xa.z + xa.w * xa.w) + (xb.x * xb.x + xb.y * xb.y) + (xb.z * xb.z + xb.w * xb.w);
;         const float u[8] = {xa.x * L.g[0].x, xa.y * L.g[0].y, xa.z * L.g[0].z, xa.w * L.g[0].w, xb.x * L.g[1].x, xb.y * L.g[1].y, xb.z * L.g[1].z, xb.w * L.g[1].w};
;         unsigned hb[8]; float lo[8];
; #pragma unroll
;         for (int j = 0; j < 8; ++j) { hb[j] = f2bf(u[j]); lo[j] = u[j] - __builtin_bit_cast(float, hb[j] << 16); }
;         const u32x4 hw = (u32x4){hb[0] | (hb[1] << 16), hb[2] | (hb[3] << 16), hb[4] | (hb[5] << 16), hb[6] | (hb[7] << 16)};
;         const u32x4 lw = (u32x4){pk2(lo[0], lo[1]), pk2(lo[2], lo[3]), pk2(lo[4], lo[5]), pk2(lo[6], lo[7])};
;         ahi[mi] = __builtin_bit_cast(bf16x8, hw); alo[mi] = __builtin_bit_cast(bf16x8, lw); }
; #pragma unroll
;     for (int n = 0; n < 5; ++n)
; #pragma unroll
;         for (int mi = 0; mi < 2; ++mi) { acc[mi][n] = __builtin_amdgcn_mfma_f32_16x16x32_bf16(ahi[mi], W.wh[n], acc[mi][n], 0, 0, 0);
;             acc[mi][n] = __builtin_amdgcn_mfma_f32_16x16x32_bf16(alo[mi], W.wh[n], acc[mi][n], 0, 0, 0);
;             acc[mi][n] = __builtin_amdgcn_mfma_f32_16x16x32_bf16(ahi[mi], W.wl[n], acc[mi][n], 0, 0, 0); }
; }
; __device__ __forceinline__ void p5_router(Frame& F) {
;     ...
; #pragma unroll 1
;           for (int ks = 0; ks < 32; ks += 2) {
;               rt_load(Lb, h0, h1, gp, (ks + 1) * 32); rt_step(La, bh, bl, acc, ss, ks * 32);
;               if (ks + 2 < 32) rt_load(La, h0, h1, gp, (ks + 2) * 32);
;               rt_step(Lb, bh, bl, acc, ss, (ks + 1) * 32); }
	v_lshlrev_b32_e32 v172, 16, v38
	v_and_b32_e32 v173, 0xffff0000, v38
	v_lshlrev_b32_e32 v174, 16, v39
	v_and_b32_e32 v175, 0xffff0000, v39
	v_lshlrev_b32_e32 v176, 16, v40
	v_and_b32_e32 v177, 0xffff0000, v40
	v_lshlrev_b32_e32 v178, 16, v41
	v_and_b32_e32 v179, 0xffff0000, v41
	v_mul_f32_e32 v180, v42, v172
	v_mul_f32_e32 v181, v43, v173
	v_mul_f32_e32 v182, v44, v174
	v_mul_f32_e32 v183, v45, v175
	v_mul_f32_e32 v184, v46, v176
	v_mul_f32_e32 v185, v47, v177
	v_mul_f32_e32 v186, v48, v178
	v_mul_f32_e32 v187, v49, v179
	v_cvt_pk_bf16_f32 v200, v180, v181
	v_cvt_pk_bf16_f32 v201, v182, v183
	v_cvt_pk_bf16_f32 v202, v184, v185
	v_cvt_pk_bf16_f32 v203, v186, v187
	v_mul_f32_e32 v196, v172, v172
	v_mul_f32_e32 v197, v174, v174
	v_mul_f32_e32 v198, v176, v176
	v_mul_f32_e32 v199, v178, v178
	v_fma_f32 v196, v173, v173, v196
	v_fma_f32 v197, v175, v175, v197
	v_fma_f32 v198, v177, v177, v198
	v_fma_f32 v199, v179, v179, v199
	v_lshlrev_b32_e32 v188, 16, v200
	v_and_b32_e32 v189, 0xffff0000, v200
	v_lshlrev_b32_e32 v190, 16, v201
	v_and_b32_e32 v191, 0xffff0000, v201
	v_lshlrev_b32_e32 v192, 16, v202
	v_and_b32_e32 v193, 0xffff0000, v202
	v_lshlrev_b32_e32 v194, 16, v203
	v_and_b32_e32 v195, 0xffff0000, v203
	v_fma_f32 v180, v42, v172, -v188
	v_fma_f32 v181, v43, v173, -v189
	v_fma_f32 v182, v44, v174, -v190
	v_fma_f32 v183, v45, v175, -v191
	v_fma_f32 v184, v46, v176, -v192
	v_fma_f32 v185, v47, v177, -v193
	v_fma_f32 v186, v48, v178, -v194
	v_fma_f32 v187, v49, v179, -v195
	v_add_f32_e32 v196, v196, v197
	v_add_f32_e32 v196, v196, v198
	v_add_f32_e32 v196, v196, v199
	v_add_f32_e32 v224, v224, v196
	v_cvt_pk_bf16_f32 v204, v180, v181
	v_cvt_pk_bf16_f32 v205, v182, v183
	v_cvt_pk_bf16_f32 v206, v184, v185
	v_cvt_pk_bf16_f32 v207, v186, v187
	s_waitcnt lgkmcnt(0)
	v_mfma_f32_16x16x32_bf16 v[18:21], v[200:203], v[58:61], v[18:21]
	v_mfma_f32_16x16x32_bf16 v[22:25], v[200:203], v[62:65], v[22:25]
	v_mfma_f32_16x16x32_bf16 v[26:29], v[200:203], v[66:69], v[26:29]
	v_mfma_f32_16x16x32_bf16 v[30:33], v[200:203], v[70:73], v[30:33]
	v_mfma_f32_16x16x32_bf16 v[34:37], v[200:203], v[74:77], v[34:37]
	v_mfma_f32_16x16x32_bf16 v[18:21], v[204:207], v[58:61], v[18:21]
	v_mfma_f32_16x16x32_bf16 v[22:25], v[204:207], v[62:65], v[22:25]
	v_mfma_f32_16x16x32_bf16 v[26:29], v[204:207], v[66:69], v[26:29]
	v_mfma_f32_16x16x32_bf16 v[30:33], v[204:207], v[70:73], v[30:33]
	v_mfma_f32_16x16x32_bf16 v[34:37], v[204:207], v[74:77], v[34:37]
	v_mfma_f32_16x16x32_bf16 v[18:21], v[200:203], v[100:103], v[18:21]
	v_mfma_f32_16x16x32_bf16 v[22:25], v[200:203], v[104:107], v[22:25]
	v_mfma_f32_16x16x32_bf16 v[26:29], v[200:203], v[108:111], v[26:29]
	v_mfma_f32_16x16x32_bf16 v[30:33], v[200:203], v[112:115], v[30:33]
	v_mfma_f32_16x16x32_bf16 v[34:37], v[200:203], v[116:119], v[34:37]
	s_barrier
	s_mov_b32 s33, s94
	s_mov_b32 s94, s95
	s_mov_b32 s95, s91
	s_mov_b32 s91, s33
	v_add_u32_e32 v216, 0x100, v216
	global_load_dwordx4 v[42:45], v216, s[66:67]
	global_load_dwordx4 v[46:49], v216, s[66:67] offset:16
	s_add_i32 m0, s91, s98
	v_add_u32_e32 v208, 0x80, v208
	global_load_lds_dwordx4 v208, s[86:87]
	s_add_i32 m0, s91, s99
	v_add_u32_e32 v209, 0x80, v209
	global_load_lds_dwordx4 v209, s[86:87]
	s_add_i32 m0, s91, s100
	v_add_u32_e32 v210, 0x80, v210
	global_load_lds_dwordx4 v210, s[86:87]
	s_add_i32 m0, s91, s101
	v_add_u32_e32 v211, 0x80, v211
	global_load_lds_dwordx4 v211, s[86:87]
	v_add_u32_e32 v214, s94, v212
	v_add_u32_e32 v215, s94, v213
	ds_read_b128 v[38:41], v215
	ds_read_b128 v[58:61], v214 offset:0
	ds_read_b128 v[62:65], v214 offset:2048
	ds_read_b128 v[66:69], v214 offset:4096
	ds_read_b128 v[70:73], v214 offset:6144
	ds_read_b128 v[74:77], v214 offset:8192
	ds_read_b128 v[100:103], v214 offset:10240
	ds_read_b128 v[104:107], v214 offset:12288
	ds_read_b128 v[108:111], v214 offset:14336
	ds_read_b128 v[112:115], v214 offset:16384
	ds_read_b128 v[116:119], v214 offset:18432
	s_waitcnt vmcnt(10)
	s_waitcnt lgkmcnt(10)
	v_lshlrev_b32_e32 v172, 16, v38
	v_and_b32_e32 v173, 0xffff0000, v38
	v_lshlrev_b32_e32 v174, 16, v39
	v_and_b32_e32 v175, 0xffff0000, v39
	v_lshlrev_b32_e32 v176, 16, v40
	v_and_b32_e32 v177, 0xffff0000, v40
	v_lshlrev_b32_e32 v178, 16, v41
	v_and_b32_e32 v179, 0xffff0000, v41
	v_mul_f32_e32 v180, v50, v172
	v_mul_f32_e32 v181, v51, v173
	v_mul_f32_e32 v182, v52, v174
	v_mul_f32_e32 v183, v53, v175
	v_mul_f32_e32 v184, v54, v176
	v_mul_f32_e32 v185, v55, v177
	v_mul_f32_e32 v186, v56, v178
	v_mul_f32_e32 v187, v57, v179
	v_cvt_pk_bf16_f32 v200, v180, v181
	v_cvt_pk_bf16_f32 v201, v182, v183
	v_cvt_pk_bf16_f32 v202, v184, v185
	v_cvt_pk_bf16_f32 v203, v186, v187
	v_mul_f32_e32 v196, v172, v172
	v_mul_f32_e32 v197, v174, v174
	v_mul_f32_e32 v198, v176, v176
	v_mul_f32_e32 v199, v178, v178
	v_fma_f32 v196, v173, v173, v196
	v_fma_f32 v197, v175, v175, v197
	v_fma_f32 v198, v177, v177, v198
	v_fma_f32 v199, v179, v179, v199
	v_lshlrev_b32_e32 v188, 16, v200
	v_and_b32_e32 v189, 0xffff0000, v200
	v_lshlrev_b32_e32 v190, 16, v201
	v_and_b32_e32 v191, 0xffff0000, v201
	v_lshlrev_b32_e32 v192, 16, v202
	v_and_b32_e32 v193, 0xffff0000, v202
	v_lshlrev_b32_e32 v194, 16, v203
	v_and_b32_e32 v195, 0xffff0000, v203
	v_fma_f32 v180, v50, v172, -v188
	v_fma_f32 v181, v51, v173, -v189
	v_fma_f32 v182, v52, v174, -v190
	v_fma_f32 v183, v53, v175, -v191
	v_fma_f32 v184, v54, v176, -v192
	v_fma_f32 v185, v55, v177, -v193
	v_fma_f32 v186, v56, v178, -v194
	v_fma_f32 v187, v57, v179, -v195
	v_add_f32_e32 v196, v196, v197
	v_add_f32_e32 v196, v196, v198
	v_add_f32_e32 v196, v196, v199
	v_add_f32_e32 v224, v224, v196
	v_cvt_pk_bf16_f32 v204, v180, v181
	v_cvt_pk_bf16_f32 v205, v182, v183
	v_cvt_pk_bf16_f32 v206, v184, v185
	v_cvt_pk_bf16_f32 v207, v186, v187
	s_waitcnt lgkmcnt(0)
	v_mfma_f32_16x16x32_bf16 v[18:21], v[200:203], v[58:61], v[18:21]
	v_mfma_f32_16x16x32_bf16 v[22:25], v[200:203], v[62:65], v[22:25]
	v_mfma_f32_16x16x32_bf16 v[26:29], v[200:203], v[66:69], v[26:29]
	v_mfma_f32_16x16x32_bf16 v[30:33], v[200:203], v[70:73], v[30:33]
	v_mfma_f32_16x16x32_bf16 v[34:37], v[200:203], v[74:77], v[34:37]
	v_mfma_f32_16x16x32_bf16 v[18:21], v[204:207], v[58:61], v[18:21]
	v_mfma_f32_16x16x32_bf16 v[22:25], v[204:207], v[62:65], v[22:25]
	v_mfma_f32_16x16x32_bf16 v[26:29], v[204:207], v[66:69], v[26:29]
	v_mfma_f32_16x16x32_bf16 v[30:33], v[204:207], v[70:73], v[30:33]
	v_mfma_f32_16x16x32_bf16 v[34:37], v[204:207], v[74:77], v[34:37]
	v_mfma_f32_16x16x32_bf16 v[18:21], v[200:203], v[100:103], v[18:21]
	v_mfma_f32_16x16x32_bf16 v[22:25], v[200:203], v[104:107], v[22:25]
	v_mfma_f32_16x16x32_bf16 v[26:29], v[200:203], v[108:111], v[26:29]
	v_mfma_f32_16x16x32_bf16 v[30:33], v[200:203], v[112:115], v[30:33]
	v_mfma_f32_16x16x32_bf16 v[34:37], v[200:203], v[116:119], v[34:37]
	s_waitcnt vmcnt(6)
	s_barrier
	s_mov_b32 s33, s94
	s_mov_b32 s94, s95
	s_mov_b32 s95, s91
	s_mov_b32 s91, s33
	s_mov_b32 s85, 30
; __device__ __forceinline__ unsigned f2bf(float f) { unsigned u = __builtin_bit_cast(unsigned, f); return (u + 0x7fffu + ((u >> 16) & 1u)) >> 16; }
; __device__ __forceinline__ void rt_step(const RtLoad& L, const bf16_t* bh, const bf16_t* bl, f32x4 (&acc)[2][5], float (&ss)[2], int ko) {
;     RtW W;
; #pragma unroll
;     for (int n = 0; n < 5; ++n) { W.wh[n] = *(const bf16x8*)(bh + (size_t)n * 16 * D + ko); W.wl[n] = *(const bf16x8*)(bl + (size_t)n * 16 * D + ko); }
;     bf16x8 ahi[2], alo[2];
; #pragma unroll
;     for (int mi = 0; mi < 2; ++mi) { const u32x4 xw = L.x[mi]; const f32x4 xa = (f32x4){bflo(xw.x), bfhi(xw.x), bflo(xw.y), bfhi(xw.y)}, xb = (f32x4){bflo(xw.z), bfhi(xw.z), bflo(xw.w), bfhi(xw.w)};
;         ss[mi] += (xa.x * xa.x + xa.y * xa.y) + (xa.z * xa.z + xa.w * xa.w) + (xb.x * xb.x + xb.y * xb.y) + (xb.z * xb.z + xb.w * xb.w);
;         const float u[8] = {xa.x * L.g[0].x, xa.y * L.g[0].y, xa.z * L.g[0].z, xa.w * L.g[0].w, xb.x * L.g[1].x, xb.y * L.g[1].y, xb.z * L.g[1].z, xb.w * L.g[1].w};
;         unsigned hb[8]; float lo[8];
; #pragma unroll
;         for (int j = 0; j < 8; ++j) { hb[j] = f2bf(u[j]); lo[j] = u[j] - __builtin_bit_cast(float, hb[j] << 16); }
;         const u32x4 hw = (u32x4){hb[0] | (hb[1] << 16), hb[2] | (hb[3] << 16), hb[4] | (hb[5] << 16), hb[6] | (hb[7] << 16)};
;         const u32x4 lw = (u32x4){pk2(lo[0], lo[1]), pk2(lo[2], lo[3]), pk2(lo[4], lo[5]), pk2(lo[6], lo[7])};
;         ahi[mi] = __builtin_bit_cast(bf16x8, hw); alo[mi] = __builtin_bit_cast(bf16x8, lw); }
; #pragma unroll
;     for (int n = 0; n < 5; ++n)
; #pragma unroll
;         for (int mi = 0; mi < 2; ++mi) { acc[mi][n] = __builtin_amdgcn_mfma_f32_16x16x32_bf16(ahi[mi], W.wh[n], acc[mi][n], 0, 0, 0);
;             acc[mi][n] = __builtin_amdgcn_mfma_f32_16x16x32_bf16(alo[mi], W.wh[n], acc[mi][n], 0, 0, 0);
;             acc[mi][n] = __builtin_amdgcn_mfma_f32_16x16x32_bf16(ahi[mi], W.wl[n], acc[mi][n], 0, 0, 0); }
; }
; __device__ __forceinline__ void p5_router(Frame& F) {
;     ...
; #pragma unroll 1
;           for (int ks = 0; ks < 32; ks += 2) {
;               rt_load(Lb, h0, h1, gp, (ks + 1) * 32); rt_step(La, bh, bl, acc, ss, ks * 32);
;               if (ks + 2 < 32) rt_load(La, h0, h1, gp, (ks + 2) * 32);
;               rt_step(Lb, bh, bl, acc, ss, (ks + 1) * 32); }
.Lrt_loop_p4:
	v_add_u32_e32 v216, 0x100, v216
	global_load_dwordx4 v[50:53], v216, s[66:67]
	global_load_dwordx4 v[54:57], v216, s[66:67] offset:16
	s_add_i32 m0, s91, s98
	v_add_u32_e32 v208, 0x80, v208
	global_load_lds_dwordx4 v208, s[86:87]
	s_add_i32 m0, s91, s99
	v_add_u32_e32 v209, 0x80, v209
	global_load_lds_dwordx4 v209, s[86:87]
	s_add_i32 m0, s91, s100
	v_add_u32_e32 v210, 0x80, v210
	global_load_lds_dwordx4 v210, s[86:87]
	s_add_i32 m0, s91, s101
	v_add_u32_e32 v211, 0x80, v211
	global_load_lds_dwordx4 v211, s[86:87]
	v_add_u32_e32 v214, s94, v212
	v_add_u32_e32 v215, s94, v213
	ds_read_b128 v[38:41], v215
	ds_read_b128 v[58:61], v214 offset:0
	ds_read_b128 v[62:65], v214 offset:2048
	ds_read_b128 v[66:69], v214 offset:4096
	ds_read_b128 v[70:73], v214 offset:6144
	ds_read_b128 v[74:77], v214 offset:8192
	ds_read_b128 v[100:103], v214 offset:10240
	ds_read_b128 v[104:107], v214 offset:12288
	ds_read_b128 v[108:111], v214 offset:14336
	ds_read_b128 v[112:115], v214 offset:16384
	ds_read_b128 v[116:119], v214 offset:18432
	s_waitcnt vmcnt(10)
	s_waitcnt lgkmcnt(10)
	v_lshlrev_b32_e32 v172, 16, v38
	v_and_b32_e32 v173, 0xffff0000, v38
	v_lshlrev_b32_e32 v174, 16, v39
	v_and_b32_e32 v175, 0xffff0000, v39
	v_lshlrev_b32_e32 v176, 16, v40
	v_and_b32_e32 v177, 0xffff0000, v40
	v_lshlrev_b32_e32 v178, 16, v41
	v_and_b32_e32 v179, 0xffff0000, v41
	v_mul_f32_e32 v180, v42, v172
	v_mul_f32_e32 v181, v43, v173
	v_mul_f32_e32 v182, v44, v174
	v_mul_f32_e32 v183, v45, v175
	v_mul_f32_e32 v184, v46, v176
	v_mul_f32_e32 v185, v47, v177
	v_mul_f32_e32 v186, v48, v178
	v_mul_f32_e32 v187, v49, v179
	v_cvt_pk_bf16_f32 v200, v180, v181
	v_cvt_pk_bf16_f32 v201, v182, v183
	v_cvt_pk_bf16_f32 v202, v184, v185
	v_cvt_pk_bf16_f32 v203, v186, v187
	v_mul_f32_e32 v196, v172, v172
	v_mul_f32_e32 v197, v174, v174
	v_mul_f32_e32 v198, v176, v176
	v_mul_f32_e32 v199, v178, v178
	v_fma_f32 v196, v173, v173, v196
	v_fma_f32 v197, v175, v175, v197
	v_fma_f32 v198, v177, v177, v198
	v_fma_f32 v199, v179, v179, v199
	v_lshlrev_b32_e32 v188, 16, v200
	v_and_b32_e32 v189, 0xffff0000, v200
	v_lshlrev_b32_e32 v190, 16, v201
	v_and_b32_e32 v191, 0xffff0000, v201
	v_lshlrev_b32_e32 v192, 16, v202
	v_and_b32_e32 v193, 0xffff0000, v202
	v_lshlrev_b32_e32 v194, 16, v203
	v_and_b32_e32 v195, 0xffff0000, v203
	v_fma_f32 v180, v42, v172, -v188
	v_fma_f32 v181, v43, v173, -v189
	v_fma_f32 v182, v44, v174, -v190
	v_fma_f32 v183, v45, v175, -v191
	v_fma_f32 v184, v46, v176, -v192
	v_fma_f32 v185, v47, v177, -v193
	v_fma_f32 v186, v48, v178, -v194
	v_fma_f32 v187, v49, v179, -v195
	v_add_f32_e32 v196, v196, v197
	v_add_f32_e32 v196, v196, v198
	v_add_f32_e32 v196, v196, v199
	v_add_f32_e32 v224, v224, v196
	v_cvt_pk_bf16_f32 v204, v180, v181
	v_cvt_pk_bf16_f32 v205, v182, v183
	v_cvt_pk_bf16_f32 v206, v184, v185
	v_cvt_pk_bf16_f32 v207, v186, v187
	s_waitcnt lgkmcnt(0)
	v_mfma_f32_16x16x32_bf16 v[18:21], v[200:203], v[58:61], v[18:21]
	v_mfma_f32_16x16x32_bf16 v[22:25], v[200:203], v[62:65], v[22:25]
	v_mfma_f32_16x16x32_bf16 v[26:29], v[200:203], v[66:69], v[26:29]
	v_mfma_f32_16x16x32_bf16 v[30:33], v[200:203], v[70:73], v[30:33]
	v_mfma_f32_16x16x32_bf16 v[34:37], v[200:203], v[74:77], v[34:37]
	v_mfma_f32_16x16x32_bf16 v[18:21], v[204:207], v[58:61], v[18:21]
	v_mfma_f32_16x16x32_bf16 v[22:25], v[204:207], v[62:65], v[22:25]
	v_mfma_f32_16x16x32_bf16 v[26:29], v[204:207], v[66:69], v[26:29]
	v_mfma_f32_16x16x32_bf16 v[30:33], v[204:207], v[70:73], v[30:33]
	v_mfma_f32_16x16x32_bf16 v[34:37], v[204:207], v[74:77], v[34:37]
	v_mfma_f32_16x16x32_bf16 v[18:21], v[200:203], v[100:103], v[18:21]
	v_mfma_f32_16x16x32_bf16 v[22:25], v[200:203], v[104:107], v[22:25]
	v_mfma_f32_16x16x32_bf16 v[26:29], v[200:203], v[108:111], v[26:29]
	v_mfma_f32_16x16x32_bf16 v[30:33], v[200:203], v[112:115], v[30:33]
	v_mfma_f32_16x16x32_bf16 v[34:37], v[200:203], v[116:119], v[34:37]
	s_waitcnt vmcnt(6)
	s_barrier
	s_mov_b32 s33, s94
	s_mov_b32 s94, s95
	s_mov_b32 s95, s91
	s_mov_b32 s91, s33
	v_add_u32_e32 v216, 0x100, v216
	global_load_dwordx4 v[42:45], v216, s[66:67]
	global_load_dwordx4 v[46:49], v216, s[66:67] offset:16
	s_add_i32 m0, s91, s98
	v_add_u32_e32 v208, 0x80, v208
	global_load_lds_dwordx4 v208, s[86:87]
	s_add_i32 m0, s91, s99
	v_add_u32_e32 v209, 0x80, v209
	global_load_lds_dwordx4 v209, s[86:87]
	s_add_i32 m0, s91, s100
	v_add_u32_e32 v210, 0x80, v210
	global_load_lds_dwordx4 v210, s[86:87]
	s_add_i32 m0, s91, s101
	v_add_u32_e32 v211, 0x80, v211
	global_load_lds_dwordx4 v211, s[86:87]
	v_add_u32_e32 v214, s94, v212
	v_add_u32_e32 v215, s94, v213
	ds_read_b128 v[38:41], v215
	ds_read_b128 v[58:61], v214 offset:0
	ds_read_b128 v[62:65], v214 offset:2048
	ds_read_b128 v[66:69], v214 offset:4096
	ds_read_b128 v[70:73], v214 offset:6144
	ds_read_b128 v[74:77], v214 offset:8192
	ds_read_b128 v[100:103], v214 offset:10240
	ds_read_b128 v[104:107], v214 offset:12288
	ds_read_b128 v[108:111], v214 offset:14336
	ds_read_b128 v[112:115], v214 offset:16384
	ds_read_b128 v[116:119], v214 offset:18432
	s_waitcnt vmcnt(10)
	s_waitcnt lgkmcnt(10)
; __device__ __forceinline__ unsigned f2bf(float f) { unsigned u = __builtin_bit_cast(unsigned, f); return (u + 0x7fffu + ((u >> 16) & 1u)) >> 16; }
; __device__ __forceinline__ void rt_step(const RtLoad& L, const bf16_t* bh, const bf16_t* bl, f32x4 (&acc)[2][5], float (&ss)[2], int ko) {
;     RtW W;
; #pragma unroll
;     for (int n = 0; n < 5; ++n) { W.wh[n] = *(const bf16x8*)(bh + (size_t)n * 16 * D + ko); W.wl[n] = *(const bf16x8*)(bl + (size_t)n * 16 * D + ko); }
;     bf16x8 ahi[2], alo[2];
; #pragma unroll
;     for (int mi = 0; mi < 2; ++mi) { const u32x4 xw = L.x[mi]; const f32x4 xa = (f32x4){bflo(xw.x), bfhi(xw.x), bflo(xw.y), bfhi(xw.y)}, xb = (f32x4){bflo(xw.z), bfhi(xw.z), bflo(xw.w), bfhi(xw.w)};
;         ss[mi] += (xa.x * xa.x + xa.y * xa.y) + (xa.z * xa.z + xa.w * xa.w) + (xb.x * xb.x + xb.y * xb.y) + (xb.z * xb.z + xb.w * xb.w);
;         const float u[8] = {xa.x * L.g[0].x, xa.y * L.g[0].y, xa.z * L.g[0].z, xa.w * L.g[0].w, xb.x * L.g[1].x, xb.y * L.g[1].y, xb.z * L.g[1].z, xb.w * L.g[1].w};
;         unsigned hb[8]; float lo[8];
; #pragma unroll
;         for (int j = 0; j < 8; ++j) { hb[j] = f2bf(u[j]); lo[j] = u[j] - __builtin_bit_cast(float, hb[j] << 16); }
;         const u32x4 hw = (u32x4){hb[0] | (hb[1] << 16), hb[2] | (hb[3] << 16), hb[4] | (hb[5] << 16), hb[6] | (hb[7] << 16)};
;         const u32x4 lw = (u32x4){pk2(lo[0], lo[1]), pk2(lo[2], lo[3]), pk2(lo[4], lo[5]), pk2(lo[6], lo[7])};
;         ahi[mi] = __builtin_bit_cast(bf16x8, hw); alo[mi] = __builtin_bit_cast(bf16x8, lw); }
; #pragma unroll
;     for (int n = 0; n < 5; ++n)
; #pragma unroll
;         for (int mi = 0; mi < 2; ++mi) { acc[mi][n] = __builtin_amdgcn_mfma_f32_16x16x32_bf16(ahi[mi], W.wh[n], acc[mi][n], 0, 0, 0);
;             acc[mi][n] = __builtin_amdgcn_mfma_f32_16x16x32_bf16(alo[mi], W.wh[n], acc[mi][n], 0, 0, 0);
;             acc[mi][n] = __builtin_amdgcn_mfma_f32_16x16x32_bf16(ahi[mi], W.wl[n], acc[mi][n], 0, 0, 0); }
; }
; __device__ __forceinline__ void p5_router(Frame& F) {
;     ...
; #pragma unroll 1
;           for (int ks = 0; ks < 32; ks += 2) {
;               rt_load(Lb, h0, h1, gp, (ks + 1) * 32); rt_step(La, bh, bl, acc, ss, ks * 32);
;               if (ks + 2 < 32) rt_load(La, h0, h1, gp, (ks + 2) * 32);
;               rt_step(Lb, bh, bl, acc, ss, (ks + 1) * 32); }
	v_lshlrev_b32_e32 v172, 16, v38
	v_and_b32_e32 v173, 0xffff0000, v38
	v_lshlrev_b32_e32 v174, 16, v39
	v_and_b32_e32 v175, 0xffff0000, v39
	v_lshlrev_b32_e32 v176, 16, v40
	v_and_b32_e32 v177, 0xffff0000, v40
	v_lshlrev_b32_e32 v178, 16, v41
	v_and_b32_e32 v179, 0xffff0000, v41
	v_mul_f32_e32 v180, v50, v172
	v_mul_f32_e32 v181, v51, v173
	v_mul_f32_e32 v182, v52, v174
	v_mul_f32_e32 v183, v53, v175
	v_mul_f32_e32 v184, v54, v176
	v_mul_f32_e32 v185, v55, v177
	v_mul_f32_e32 v186, v56, v178
	v_mul_f32_e32 v187, v57, v179
	v_cvt_pk_bf16_f32 v200, v180, v181
	v_cvt_pk_bf16_f32 v201, v182, v183
	v_cvt_pk_bf16_f32 v202, v184, v185
	v_cvt_pk_bf16_f32 v203, v186, v187
	v_mul_f32_e32 v196, v172, v172
	v_mul_f32_e32 v197, v174, v174
	v_mul_f32_e32 v198, v176, v176
	v_mul_f32_e32 v199, v178, v178
	v_fma_f32 v196, v173, v173, v196
	v_fma_f32 v197, v175, v175, v197
	v_fma_f32 v198, v177, v177, v198
	v_fma_f32 v199, v179, v179, v199
	v_lshlrev_b32_e32 v188, 16, v200
	v_and_b32_e32 v189, 0xffff0000, v200
	v_lshlrev_b32_e32 v190, 16, v201
	v_and_b32_e32 v191, 0xffff0000, v201
	v_lshlrev_b32_e32 v192, 16, v202
	v_and_b32_e32 v193, 0xffff0000, v202
	v_lshlrev_b32_e32 v194, 16, v203
	v_and_b32_e32 v195, 0xffff0000, v203
	v_fma_f32 v180, v50, v172, -v188
	v_fma_f32 v181, v51, v173, -v189
	v_fma_f32 v182, v52, v174, -v190
	v_fma_f32 v183, v53, v175, -v191
	v_fma_f32 v184, v54, v176, -v192
	v_fma_f32 v185, v55, v177, -v193
	v_fma_f32 v186, v56, v178, -v194
	v_fma_f32 v187, v57, v179, -v195
	v_add_f32_e32 v196, v196, v197
	v_add_f32_e32 v196, v196, v198
	v_add_f32_e32 v196, v196, v199
	v_add_f32_e32 v224, v224, v196
	v_cvt_pk_bf16_f32 v204, v180, v181
	v_cvt_pk_bf16_f32 v205, v182, v183
	v_cvt_pk_bf16_f32 v206, v184, v185
	v_cvt_pk_bf16_f32 v207, v186, v187
	s_waitcnt lgkmcnt(0)
	v_mfma_f32_16x16x32_bf16 v[18:21], v[200:203], v[58:61], v[18:21]
	v_mfma_f32_16x16x32_bf16 v[22:25], v[200:203], v[62:65], v[22:25]
	v_mfma_f32_16x16x32_bf16 v[26:29], v[200:203], v[66:69], v[26:29]
	v_mfma_f32_16x16x32_bf16 v[30:33], v[200:203], v[70:73], v[30:33]
	v_mfma_f32_16x16x32_bf16 v[34:37], v[200:203], v[74:77], v[34:37]
	v_mfma_f32_16x16x32_bf16 v[18:21], v[204:207], v[58:61], v[18:21]
	v_mfma_f32_16x16x32_bf16 v[22:25], v[204:207], v[62:65], v[22:25]
	v_mfma_f32_16x16x32_bf16 v[26:29], v[204:207], v[66:69], v[26:29]
	v_mfma_f32_16x16x32_bf16 v[30:33], v[204:207], v[70:73], v[30:33]
	v_mfma_f32_16x16x32_bf16 v[34:37], v[204:207], v[74:77], v[34:37]
	v_mfma_f32_16x16x32_bf16 v[18:21], v[200:203], v[100:103], v[18:21]
	v_mfma_f32_16x16x32_bf16 v[22:25], v[200:203], v[104:107], v[22:25]
	v_mfma_f32_16x16x32_bf16 v[26:29], v[200:203], v[108:111], v[26:29]
	v_mfma_f32_16x16x32_bf16 v[30:33], v[200:203], v[112:115], v[30:33]
	v_mfma_f32_16x16x32_bf16 v[34:37], v[200:203], v[116:119], v[34:37]
	s_waitcnt vmcnt(6)
	s_barrier
	s_mov_b32 s33, s94
	s_mov_b32 s94, s95
	s_mov_b32 s95, s91
	s_mov_b32 s91, s33
	s_sub_u32 s85, s85, 1
	s_cmp_lg_u32 s85, 0
	s_cbranch_scc1 .Lrt_loop_p4
	v_add_u32_e32 v216, 0x100, v216
	global_load_dwordx4 v[50:53], v216, s[66:67]
	global_load_dwordx4 v[54:57], v216, s[66:67] offset:16
	v_add_u32_e32 v214, s94, v212
	v_add_u32_e32 v215, s94, v213
	ds_read_b128 v[38:41], v215
	ds_read_b128 v[58:61], v214 offset:0
	ds_read_b128 v[62:65], v214 offset:2048
	ds_read_b128 v[66:69], v214 offset:4096
	ds_read_b128 v[70:73], v214 offset:6144
	ds_read_b128 v[74:77], v214 offset:8192
	ds_read_b128 v[100:103], v214 offset:10240
	ds_read_b128 v[104:107], v214 offset:12288
	ds_read_b128 v[108:111], v214 offset:14336
	ds_read_b128 v[112:115], v214 offset:16384
	ds_read_b128 v[116:119], v214 offset:18432
	s_waitcnt vmcnt(6)
	s_waitcnt lgkmcnt(10)
	v_lshlrev_b32_e32 v172, 16, v38
	v_and_b32_e32 v173, 0xffff0000, v38
	v_lshlrev_b32_e32 v174, 16, v39
	v_and_b32_e32 v175, 0xffff0000, v39
	v_lshlrev_b32_e32 v176, 16, v40
	v_and_b32_e32 v177, 0xffff0000, v40
	v_lshlrev_b32_e32 v178, 16, v41
	v_and_b32_e32 v179, 0xffff0000, v41
	v_mul_f32_e32 v180, v42, v172
	v_mul_f32_e32 v181, v43, v173
	v_mul_f32_e32 v182, v44, v174
	v_mul_f32_e32 v183, v45, v175
	v_mul_f32_e32 v184, v46, v176
	v_mul_f32_e32 v185, v47, v177
	v_mul_f32_e32 v186, v48, v178
	v_mul_f32_e32 v187, v49, v179
	v_cvt_pk_bf16_f32 v200, v180, v181
	v_cvt_pk_bf16_f32 v201, v182, v183
	v_cvt_pk_bf16_f32 v202, v184, v185
	v_cvt_pk_bf16_f32 v203, v186, v187
	v_mul_f32_e32 v196, v172, v172
	v_mul_f32_e32 v197, v174, v174
	v_mul_f32_e32 v198, v176, v176
	v_mul_f32_e32 v199, v178, v178
	v_fma_f32 v196, v173, v173, v196
	v_fma_f32 v197, v175, v175, v197
	v_fma_f32 v198, v177, v177, v198
	v_fma_f32 v199, v179, v179, v199
	v_lshlrev_b32_e32 v188, 16, v200
	v_and_b32_e32 v189, 0xffff0000, v200
	v_lshlrev_b32_e32 v190, 16, v201
	v_and_b32_e32 v191, 0xffff0000, v201
	v_lshlrev_b32_e32 v192, 16, v202
	v_and_b32_e32 v193, 0xffff0000, v202
	v_lshlrev_b32_e32 v194, 16, v203
	v_and_b32_e32 v195, 0xffff0000, v203
	v_fma_f32 v180, v42, v172, -v188
	v_fma_f32 v181, v43, v173, -v189
	v_fma_f32 v182, v44, v174, -v190
	v_fma_f32 v183, v45, v175, -v191
	v_fma_f32 v184, v46, v176, -v192
	v_fma_f32 v185, v47, v177, -v193
	v_fma_f32 v186, v48, v178, -v194
	v_fma_f32 v187, v49, v179, -v195
	v_add_f32_e32 v196, v196, v197
	v_add_f32_e32 v196, v196, v198
	v_add_f32_e32 v196, v196, v199
	v_add_f32_e32 v224, v224, v196
	v_cvt_pk_bf16_f32 v204, v180, v181
	v_cvt_pk_bf16_f32 v205, v182, v183
	v_cvt_pk_bf16_f32 v206, v184, v185
	v_cvt_pk_bf16_f32 v207, v186, v187
	s_waitcnt lgkmcnt(0)
	v_mfma_f32_16x16x32_bf16 v[18:21], v[200:203], v[58:61], v[18:21]
	v_mfma_f32_16x16x32_bf16 v[22:25], v[200:203], v[62:65], v[22:25]
	v_mfma_f32_16x16x32_bf16 v[26:29], v[200:203], v[66:69], v[26:29]
	v_mfma_f32_16x16x32_bf16 v[30:33], v[200:203], v[70:73], v[30:33]
	v_mfma_f32_16x16x32_bf16 v[34:37], v[200:203], v[74:77], v[34:37]
	v_mfma_f32_16x16x32_bf16 v[18:21], v[204:207], v[58:61], v[18:21]
	v_mfma_f32_16x16x32_bf16 v[22:25], v[204:207], v[62:65], v[22:25]
	v_mfma_f32_16x16x32_bf16 v[26:29], v[204:207], v[66:69], v[26:29]
	v_mfma_f32_16x16x32_bf16 v[30:33], v[204:207], v[70:73], v[30:33]
	v_mfma_f32_16x16x32_bf16 v[34:37], v[204:207], v[74:77], v[34:37]
	v_mfma_f32_16x16x32_bf16 v[18:21], v[200:203], v[100:103], v[18:21]
	v_mfma_f32_16x16x32_bf16 v[22:25], v[200:203], v[104:107], v[22:25]
	v_mfma_f32_16x16x32_bf16 v[26:29], v[200:203], v[108:111], v[26:29]
	v_mfma_f32_16x16x32_bf16 v[30:33], v[200:203], v[112:115], v[30:33]
	v_mfma_f32_16x16x32_bf16 v[34:37], v[200:203], v[116:119], v[34:37]
	s_waitcnt vmcnt(2)
	s_barrier
; __device__ __forceinline__ unsigned f2bf(float f) { unsigned u = __builtin_bit_cast(unsigned, f); return (u + 0x7fffu + ((u >> 16) & 1u)) >> 16; }
; __device__ __forceinline__ void rt_step(const RtLoad& L, const bf16_t* bh, const bf16_t* bl, f32x4 (&acc)[2][5], float (&ss)[2], int ko) {
;     RtW W;
; #pragma unroll
;     for (int n = 0; n < 5; ++n) { W.wh[n] = *(const bf16x8*)(bh + (size_t)n * 16 * D + ko); W.wl[n] = *(const bf16x8*)(bl + (size_t)n * 16 * D + ko); }
;     bf16x8 ahi[2], alo[2];
; #pragma unroll
;     for (int mi = 0; mi < 2; ++mi) { const u32x4 xw = L.x[mi]; const f32x4 xa = (f32x4){bflo(xw.x), bfhi(xw.x), bflo(xw.y), bfhi(xw.y)}, xb = (f32x4){bflo(xw.z), bfhi(xw.z), bflo(xw.w), bfhi(xw.w)};
;         ss[mi] += (xa.x * xa.x + xa.y * xa.y) + (xa.z * xa.z + xa.w * xa.w) + (xb.x * xb.x + xb.y * xb.y) + (xb.z * xb.z + xb.w * xb.w);
;         const float u[8] = {xa.x * L.g[0].x, xa.y * L.g[0].y, xa.z * L.g[0].z, xa.w * L.g[0].w, xb.x * L.g[1].x, xb.y * L.g[1].y, xb.z * L.g[1].z, xb.w * L.g[1].w};
;         unsigned hb[8]; float lo[8];
; #pragma unroll
;         for (int j = 0; j < 8; ++j) { hb[j] = f2bf(u[j]); lo[j] = u[j] - __builtin_bit_cast(float, hb[j] << 16); }
;         const u32x4 hw = (u32x4){hb[0] | (hb[1] << 16), hb[2] | (hb[3] << 16), hb[4] | (hb[5] << 16), hb[6] | (hb[7] << 16)};
;         const u32x4 lw = (u32x4){pk2(lo[0], lo[1]), pk2(lo[2], lo[3]), pk2(lo[4], lo[5]), pk2(lo[6], lo[7])};
;         ahi[mi] = __builtin_bit_cast(bf16x8, hw); alo[mi] = __builtin_bit_cast(bf16x8, lw); }
; #pragma unroll
;     for (int n = 0; n < 5; ++n)
; #pragma unroll
;         for (int mi = 0; mi < 2; ++mi) { acc[mi][n] = __builtin_amdgcn_mfma_f32_16x16x32_bf16(ahi[mi], W.wh[n], acc[mi][n], 0, 0, 0);
;             acc[mi][n] = __builtin_amdgcn_mfma_f32_16x16x32_bf16(alo[mi], W.wh[n], acc[mi][n], 0, 0, 0);
;             acc[mi][n] = __builtin_amdgcn_mfma_f32_16x16x32_bf16(ahi[mi], W.wl[n], acc[mi][n], 0, 0, 0); }
; }
; __device__ __forceinline__ void p5_router(Frame& F) {
;     ...
; #pragma unroll 1
;           for (int ks = 0; ks < 32; ks += 2) {
;               rt_load(Lb, h0, h1, gp, (ks + 1) * 32); rt_step(La, bh, bl, acc, ss, ks * 32);
;               if (ks + 2 < 32) rt_load(La, h0, h1, gp, (ks + 2) * 32);
;               rt_step(Lb, bh, bl, acc, ss, (ks + 1) * 32); }
	s_mov_b32 s33, s94
	s_mov_b32 s94, s95
	s_mov_b32 s95, s91
	s_mov_b32 s91, s33
	v_add_u32_e32 v214, s94, v212
	v_add_u32_e32 v215, s94, v213
	ds_read_b128 v[38:41], v215
	ds_read_b128 v[58:61], v214 offset:0
	ds_read_b128 v[62:65], v214 offset:2048
	ds_read_b128 v[66:69], v214 offset:4096
	ds_read_b128 v[70:73], v214 offset:6144
	ds_read_b128 v[74:77], v214 offset:8192
	ds_read_b128 v[100:103], v214 offset:10240
	ds_read_b128 v[104:107], v214 offset:12288
	ds_read_b128 v[108:111], v214 offset:14336
	ds_read_b128 v[112:115], v214 offset:16384
	ds_read_b128 v[116:119], v214 offset:18432
	s_waitcnt vmcnt(0)
	s_waitcnt lgkmcnt(10)
	v_lshlrev_b32_e32 v172, 16, v38
	v_and_b32_e32 v173, 0xffff0000, v38
	v_lshlrev_b32_e32 v174, 16, v39
	v_and_b32_e32 v175, 0xffff0000, v39
	v_lshlrev_b32_e32 v176, 16, v40
	v_and_b32_e32 v177, 0xffff0000, v40
	v_lshlrev_b32_e32 v178, 16, v41
	v_and_b32_e32 v179, 0xffff0000, v41
	v_mul_f32_e32 v180, v50, v172
	v_mul_f32_e32 v181, v51, v173
	v_mul_f32_e32 v182, v52, v174
	v_mul_f32_e32 v183, v53, v175
	v_mul_f32_e32 v184, v54, v176
	v_mul_f32_e32 v185, v55, v177
	v_mul_f32_e32 v186, v56, v178
	v_mul_f32_e32 v187, v57, v179
	v_cvt_pk_bf16_f32 v200, v180, v181
	v_cvt_pk_bf16_f32 v201, v182, v183
	v_cvt_pk_bf16_f32 v202, v184, v185
	v_cvt_pk_bf16_f32 v203, v186, v187
	v_mul_f32_e32 v196, v172, v172
	v_mul_f32_e32 v197, v174, v174
	v_mul_f32_e32 v198, v176, v176
	v_mul_f32_e32 v199, v178, v178
	v_fma_f32 v196, v173, v173, v196
	v_fma_f32 v197, v175, v175, v197
	v_fma_f32 v198, v177, v177, v198
	v_fma_f32 v199, v179, v179, v199
	v_lshlrev_b32_e32 v188, 16, v200
	v_and_b32_e32 v189, 0xffff0000, v200
	v_lshlrev_b32_e32 v190, 16, v201
	v_and_b32_e32 v191, 0xffff0000, v201
	v_lshlrev_b32_e32 v192, 16, v202
	v_and_b32_e32 v193, 0xffff0000, v202
	v_lshlrev_b32_e32 v194, 16, v203
	v_and_b32_e32 v195, 0xffff0000, v203
	v_fma_f32 v180, v50, v172, -v188
	v_fma_f32 v181, v51, v173, -v189
	v_fma_f32 v182, v52, v174, -v190
	v_fma_f32 v183, v53, v175, -v191
	v_fma_f32 v184, v54, v176, -v192
	v_fma_f32 v185, v55, v177, -v193
	v_fma_f32 v186, v56, v178, -v194
	v_fma_f32 v187, v57, v179, -v195
	v_add_f32_e32 v196, v196, v197
	v_add_f32_e32 v196, v196, v198
	v_add_f32_e32 v196, v196, v199
	v_add_f32_e32 v224, v224, v196
	v_cvt_pk_bf16_f32 v204, v180, v181
	v_cvt_pk_bf16_f32 v205, v182, v183
	v_cvt_pk_bf16_f32 v206, v184, v185
	v_cvt_pk_bf16_f32 v207, v186, v187
	s_waitcnt lgkmcnt(0)
	v_mfma_f32_16x16x32_bf16 v[18:21], v[200:203], v[58:61], v[18:21]
	v_mfma_f32_16x16x32_bf16 v[22:25], v[200:203], v[62:65], v[22:25]
	v_mfma_f32_16x16x32_bf16 v[26:29], v[200:203], v[66:69], v[26:29]
	v_mfma_f32_16x16x32_bf16 v[30:33], v[200:203], v[70:73], v[30:33]
	v_mfma_f32_16x16x32_bf16 v[34:37], v[200:203], v[74:77], v[34:37]
	v_mfma_f32_16x16x32_bf16 v[18:21], v[204:207], v[58:61], v[18:21]
	v_mfma_f32_16x16x32_bf16 v[22:25], v[204:207], v[62:65], v[22:25]
	v_mfma_f32_16x16x32_bf16 v[26:29], v[204:207], v[66:69], v[26:29]
	v_mfma_f32_16x16x32_bf16 v[30:33], v[204:207], v[70:73], v[30:33]
	v_mfma_f32_16x16x32_bf16 v[34:37], v[204:207], v[74:77], v[34:37]
	v_mfma_f32_16x16x32_bf16 v[18:21], v[200:203], v[100:103], v[18:21]
	v_mfma_f32_16x16x32_bf16 v[22:25], v[200:203], v[104:107], v[22:25]
	v_mfma_f32_16x16x32_bf16 v[26:29], v[200:203], v[108:111], v[26:29]
	v_mfma_f32_16x16x32_bf16 v[30:33], v[200:203], v[112:115], v[30:33]
	v_mfma_f32_16x16x32_bf16 v[34:37], v[200:203], v[116:119], v[34:37]
	s_barrier
	s_mov_b32 s33, s94
	s_mov_b32 s94, s95
	s_mov_b32 s95, s91
	s_mov_b32 s91, s33
	s_branch .Lrt_out
.Lrt_path3:
	v_add_u32_e32 v216, 0x100, v216
	global_load_dwordx4 v[50:53], v216, s[66:67]
	global_load_dwordx4 v[54:57], v216, s[66:67] offset:16
	s_add_i32 m0, s91, s98
	v_add_u32_e32 v208, 0x80, v208
	global_load_lds_dwordx4 v208, s[86:87]
	s_add_i32 m0, s91, s99
	v_add_u32_e32 v209, 0x80, v209
	global_load_lds_dwordx4 v209, s[86:87]
	s_add_i32 m0, s91, s100
	v_add_u32_e32 v210, 0x80, v210
	global_load_lds_dwordx4 v210, s[86:87]
	v_add_u32_e32 v214, s94, v212
	v_add_u32_e32 v215, s94, v213
	ds_read_b128 v[38:41], v215
	ds_read_b128 v[58:61], v214 offset:0
	ds_read_b128 v[62:65], v214 offset:2048
	ds_read_b128 v[66:69], v214 offset:4096
	ds_read_b128 v[70:73], v214 offset:6144
	ds_read_b128 v[74:77], v214 offset:8192
	ds_read_b128 v[100:103], v214 offset:10240
	ds_read_b128 v[104:107], v214 offset:12288
	ds_read_b128 v[108:111], v214 offset:14336
	ds_read_b128 v[112:115], v214 offset:16384
	ds_read_b128 v[116:119], v214 offset:18432
	s_waitcnt lgkmcnt(10)
	v_lshlrev_b32_e32 v172, 16, v38
	v_and_b32_e32 v173, 0xffff0000, v38
	v_lshlrev_b32_e32 v174, 16, v39
	v_and_b32_e32 v175, 0xffff0000, v39
	v_lshlrev_b32_e32 v176, 16, v40
	v_and_b32_e32 v177, 0xffff0000, v40
	v_lshlrev_b32_e32 v178, 16, v41
	v_and_b32_e32 v179, 0xffff0000, v41
	v_mul_f32_e32 v180, v42, v172
	v_mul_f32_e32 v181, v43, v173
	v_mul_f32_e32 v182, v44, v174
	v_mul_f32_e32 v183, v45, v175
	v_mul_f32_e32 v184, v46, v176
	v_mul_f32_e32 v185, v47, v177
	v_mul_f32_e32 v186, v48, v178
	v_mul_f32_e32 v187, v49, v179
	v_cvt_pk_bf16_f32 v200, v180, v181
	v_cvt_pk_bf16_f32 v201, v182, v183
	v_cvt_pk_bf16_f32 v202, v184, v185
	v_cvt_pk_bf16_f32 v203, v186, v187
	v_mul_f32_e32 v196, v172, v172
	v_mul_f32_e32 v197, v174, v174
	v_mul_f32_e32 v198, v176, v176
	v_mul_f32_e32 v199, v178, v178
	v_fma_f32 v196, v173, v173, v196
	v_fma_f32 v197, v175, v175, v197
	v_fma_f32 v198, v177, v177, v198
	v_fma_f32 v199, v179, v179, v199
	v_lshlrev_b32_e32 v188, 16, v200
	v_and_b32_e32 v189, 0xffff0000, v200
	v_lshlrev_b32_e32 v190, 16, v201
	v_and_b32_e32 v191, 0xffff0000, v201
	v_lshlrev_b32_e32 v192, 16, v202
	v_and_b32_e32 v193, 0xffff0000, v202
	v_lshlrev_b32_e32 v194, 16, v203
	v_and_b32_e32 v195, 0xffff0000, v203
	v_fma_f32 v180, v42, v172, -v188
	v_fma_f32 v181, v43, v173, -v189
	v_fma_f32 v182, v44, v174, -v190
	v_fma_f32 v183, v45, v175, -v191
	v_fma_f32 v184, v46, v176, -v192
	v_fma_f32 v185, v47, v177, -v193
	v_fma_f32 v186, v48, v178, -v194
	v_fma_f32 v187, v49, v179, -v195
	v_add_f32_e32 v196, v196, v197
	v_add_f32_e32 v196, v196, v198
	v_add_f32_e32 v196, v196, v199
	v_add_f32_e32 v224, v224, v196
	v_cvt_pk_bf16_f32 v204, v180, v181
	v_cvt_pk_bf16_f32 v205, v182, v183
	v_cvt_pk_bf16_f32 v206, v184, v185
	v_cvt_pk_bf16_f32 v207, v186, v187
	s_waitcnt lgkmcnt(0)
; __device__ __forceinline__ unsigned f2bf(float f) { unsigned u = __builtin_bit_cast(unsigned, f); return (u + 0x7fffu + ((u >> 16) & 1u)) >> 16; }
; __device__ __forceinline__ void rt_step(const RtLoad& L, const bf16_t* bh, const bf16_t* bl, f32x4 (&acc)[2][5], float (&ss)[2], int ko) {
;     RtW W;
; #pragma unroll
;     for (int n = 0; n < 5; ++n) { W.wh[n] = *(const bf16x8*)(bh + (size_t)n * 16 * D + ko); W.wl[n] = *(const bf16x8*)(bl + (size_t)n * 16 * D + ko); }
;     bf16x8 ahi[2], alo[2];
; #pragma unroll
;     for (int mi = 0; mi < 2; ++mi) { const u32x4 xw = L.x[mi]; const f32x4 xa = (f32x4){bflo(xw.x), bfhi(xw.x), bflo(xw.y), bfhi(xw.y)}, xb = (f32x4){bflo(xw.z), bfhi(xw.z), bflo(xw.w), bfhi(xw.w)};
;         ss[mi] += (xa.x * xa.x + xa.y * xa.y) + (xa.z * xa.z + xa.w * xa.w) + (xb.x * xb.x + xb.y * xb.y) + (xb.z * xb.z + xb.w * xb.w);
;         const float u[8] = {xa.x * L.g[0].x, xa.y * L.g[0].y, xa.z * L.g[0].z, xa.w * L.g[0].w, xb.x * L.g[1].x, xb.y * L.g[1].y, xb.z * L.g[1].z, xb.w * L.g[1].w};
;         unsigned hb[8]; float lo[8];
; #pragma unroll
;         for (int j = 0; j < 8; ++j) { hb[j] = f2bf(u[j]); lo[j] = u[j] - __builtin_bit_cast(float, hb[j] << 16); }
;         const u32x4 hw = (u32x4){hb[0] | (hb[1] << 16), hb[2] | (hb[3] << 16), hb[4] | (hb[5] << 16), hb[6] | (hb[7] << 16)};
;         const u32x4 lw = (u32x4){pk2(lo[0], lo[1]), pk2(lo[2], lo[3]), pk2(lo[4], lo[5]), pk2(lo[6], lo[7])};
;         ahi[mi] = __builtin_bit_cast(bf16x8, hw); alo[mi] = __builtin_bit_cast(bf16x8, lw); }
; #pragma unroll
;     for (int n = 0; n < 5; ++n)
; #pragma unroll
;         for (int mi = 0; mi < 2; ++mi) { acc[mi][n] = __builtin_amdgcn_mfma_f32_16x16x32_bf16(ahi[mi], W.wh[n], acc[mi][n], 0, 0, 0);
;             acc[mi][n] = __builtin_amdgcn_mfma_f32_16x16x32_bf16(alo[mi], W.wh[n], acc[mi][n], 0, 0, 0);
;             acc[mi][n] = __builtin_amdgcn_mfma_f32_16x16x32_bf16(ahi[mi], W.wl[n], acc[mi][n], 0, 0, 0); }
; }
; __device__ __forceinline__ void p5_router(Frame& F) {
;     ...
; #pragma unroll 1
;           for (int ks = 0; ks < 32; ks += 2) {
;               rt_load(Lb, h0, h1, gp, (ks + 1) * 32); rt_step(La, bh, bl, acc, ss, ks * 32);
;               if (ks + 2 < 32) rt_load(La, h0, h1, gp, (ks + 2) * 32);
;               rt_step(Lb, bh, bl, acc, ss, (ks + 1) * 32); }
	v_mfma_f32_16x16x32_bf16 v[18:21], v[200:203], v[58:61], v[18:21]
	v_mfma_f32_16x16x32_bf16 v[22:25], v[200:203], v[62:65], v[22:25]
	v_mfma_f32_16x16x32_bf16 v[26:29], v[200:203], v[66:69], v[26:29]
	v_mfma_f32_16x16x32_bf16 v[30:33], v[200:203], v[70:73], v[30:33]
	v_mfma_f32_16x16x32_bf16 v[34:37], v[200:203], v[74:77], v[34:37]
	v_mfma_f32_16x16x32_bf16 v[18:21], v[204:207], v[58:61], v[18:21]
	v_mfma_f32_16x16x32_bf16 v[22:25], v[204:207], v[62:65], v[22:25]
	v_mfma_f32_16x16x32_bf16 v[26:29], v[204:207], v[66:69], v[26:29]
	v_mfma_f32_16x16x32_bf16 v[30:33], v[204:207], v[70:73], v[30:33]
	v_mfma_f32_16x16x32_bf16 v[34:37], v[204:207], v[74:77], v[34:37]
	v_mfma_f32_16x16x32_bf16 v[18:21], v[200:203], v[100:103], v[18:21]
	v_mfma_f32_16x16x32_bf16 v[22:25], v[200:203], v[104:107], v[22:25]
	v_mfma_f32_16x16x32_bf16 v[26:29], v[200:203], v[108:111], v[26:29]
	v_mfma_f32_16x16x32_bf16 v[30:33], v[200:203], v[112:115], v[30:33]
	v_mfma_f32_16x16x32_bf16 v[34:37], v[200:203], v[116:119], v[34:37]
	s_barrier
	s_mov_b32 s33, s94
	s_mov_b32 s94, s95
	s_mov_b32 s95, s91
	s_mov_b32 s91, s33
	v_add_u32_e32 v216, 0x100, v216
	global_load_dwordx4 v[42:45], v216, s[66:67]
	global_load_dwordx4 v[46:49], v216, s[66:67] offset:16
	s_add_i32 m0, s91, s98
	v_add_u32_e32 v208, 0x80, v208
	global_load_lds_dwordx4 v208, s[86:87]
	s_add_i32 m0, s91, s99
	v_add_u32_e32 v209, 0x80, v209
	global_load_lds_dwordx4 v209, s[86:87]
	s_add_i32 m0, s91, s100
	v_add_u32_e32 v210, 0x80, v210
	global_load_lds_dwordx4 v210, s[86:87]
	v_add_u32_e32 v214, s94, v212
	v_add_u32_e32 v215, s94, v213
	ds_read_b128 v[38:41], v215
	ds_read_b128 v[58:61], v214 offset:0
	ds_read_b128 v[62:65], v214 offset:2048
	ds_read_b128 v[66:69], v214 offset:4096
	ds_read_b128 v[70:73], v214 offset:6144
	ds_read_b128 v[74:77], v214 offset:8192
	ds_read_b128 v[100:103], v214 offset:10240
	ds_read_b128 v[104:107], v214 offset:12288
	ds_read_b128 v[108:111], v214 offset:14336
	ds_read_b128 v[112:115], v214 offset:16384
	ds_read_b128 v[116:119], v214 offset:18432
	s_waitcnt vmcnt(8)
	s_waitcnt lgkmcnt(10)
	v_lshlrev_b32_e32 v172, 16, v38
	v_and_b32_e32 v173, 0xffff0000, v38
	v_lshlrev_b32_e32 v174, 16, v39
	v_and_b32_e32 v175, 0xffff0000, v39
	v_lshlrev_b32_e32 v176, 16, v40
	v_and_b32_e32 v177, 0xffff0000, v40
	v_lshlrev_b32_e32 v178, 16, v41
	v_and_b32_e32 v179, 0xffff0000, v41
	v_mul_f32_e32 v180, v50, v172
	v_mul_f32_e32 v181, v51, v173
	v_mul_f32_e32 v182, v52, v174
	v_mul_f32_e32 v183, v53, v175
	v_mul_f32_e32 v184, v54, v176
	v_mul_f32_e32 v185, v55, v177
	v_mul_f32_e32 v186, v56, v178
	v_mul_f32_e32 v187, v57, v179
	v_cvt_pk_bf16_f32 v200, v180, v181
	v_cvt_pk_bf16_f32 v201, v182, v183
	v_cvt_pk_bf16_f32 v202, v184, v185
	v_cvt_pk_bf16_f32 v203, v186, v187
	v_mul_f32_e32 v196, v172, v172
	v_mul_f32_e32 v197, v174, v174
	v_mul_f32_e32 v198, v176, v176
	v_mul_f32_e32 v199, v178, v178
	v_fma_f32 v196, v173, v173, v196
	v_fma_f32 v197, v175, v175, v197
	v_fma_f32 v198, v177, v177, v198
	v_fma_f32 v199, v179, v179, v199
	v_lshlrev_b32_e32 v188, 16, v200
	v_and_b32_e32 v189, 0xffff0000, v200
	v_lshlrev_b32_e32 v190, 16, v201
	v_and_b32_e32 v191, 0xffff0000, v201
	v_lshlrev_b32_e32 v192, 16, v202
	v_and_b32_e32 v193, 0xffff0000, v202
	v_lshlrev_b32_e32 v194, 16, v203
	v_and_b32_e32 v195, 0xffff0000, v203
	v_fma_f32 v180, v50, v172, -v188
	v_fma_f32 v181, v51, v173, -v189
	v_fma_f32 v182, v52, v174, -v190
	v_fma_f32 v183, v53, v175, -v191
	v_fma_f32 v184, v54, v176, -v192
	v_fma_f32 v185, v55, v177, -v193
	v_fma_f32 v186, v56, v178, -v194
	v_fma_f32 v187, v57, v179, -v195
	v_add_f32_e32 v196, v196, v197
	v_add_f32_e32 v196, v196, v198
	v_add_f32_e32 v196, v196, v199
	v_add_f32_e32 v224, v224, v196
	v_cvt_pk_bf16_f32 v204, v180, v181
	v_cvt_pk_bf16_f32 v205, v182, v183
	v_cvt_pk_bf16_f32 v206, v184, v185
	v_cvt_pk_bf16_f32 v207, v186, v187
	s_waitcnt lgkmcnt(0)
	v_mfma_f32_16x16x32_bf16 v[18:21], v[200:203], v[58:61], v[18:21]
	v_mfma_f32_16x16x32_bf16 v[22:25], v[200:203], v[62:65], v[22:25]
	v_mfma_f32_16x16x32_bf16 v[26:29], v[200:203], v[66:69], v[26:29]
	v_mfma_f32_16x16x32_bf16 v[30:33], v[200:203], v[70:73], v[30:33]
	v_mfma_f32_16x16x32_bf16 v[34:37], v[200:203], v[74:77], v[34:37]
	v_mfma_f32_16x16x32_bf16 v[18:21], v[204:207], v[58:61], v[18:21]
	v_mfma_f32_16x16x32_bf16 v[22:25], v[204:207], v[62:65], v[22:25]
	v_mfma_f32_16x16x32_bf16 v[26:29], v[204:207], v[66:69], v[26:29]
	v_mfma_f32_16x16x32_bf16 v[30:33], v[204:207], v[70:73], v[30:33]
	v_mfma_f32_16x16x32_bf16 v[34:37], v[204:207], v[74:77], v[34:37]
	v_mfma_f32_16x16x32_bf16 v[18:21], v[200:203], v[100:103], v[18:21]
	v_mfma_f32_16x16x32_bf16 v[22:25], v[200:203], v[104:107], v[22:25]
	v_mfma_f32_16x16x32_bf16 v[26:29], v[200:203], v[108:111], v[26:29]
	v_mfma_f32_16x16x32_bf16 v[30:33], v[200:203], v[112:115], v[30:33]
	v_mfma_f32_16x16x32_bf16 v[34:37], v[200:203], v[116:119], v[34:37]
	s_waitcnt vmcnt(5)
	s_barrier
	s_mov_b32 s33, s94
	s_mov_b32 s94, s95
	s_mov_b32 s95, s91
	s_mov_b32 s91, s33
	s_mov_b32 s85, 30
; __device__ __forceinline__ unsigned f2bf(float f) { unsigned u = __builtin_bit_cast(unsigned, f); return (u + 0x7fffu + ((u >> 16) & 1u)) >> 16; }
; __device__ __forceinline__ void rt_step(const RtLoad& L, const bf16_t* bh, const bf16_t* bl, f32x4 (&acc)[2][5], float (&ss)[2], int ko) {
;     RtW W;
; #pragma unroll
;     for (int n = 0; n < 5; ++n) { W.wh[n] = *(const bf16x8*)(bh + (size_t)n * 16 * D + ko); W.wl[n] = *(const bf16x8*)(bl + (size_t)n * 16 * D + ko); }
;     bf16x8 ahi[2], alo[2];
; #pragma unroll
;     for (int mi = 0; mi < 2; ++mi) { const u32x4 xw = L.x[mi]; const f32x4 xa = (f32x4){bflo(xw.x), bfhi(xw.x), bflo(xw.y), bfhi(xw.y)}, xb = (f32x4){bflo(xw.z), bfhi(xw.z), bflo(xw.w), bfhi(xw.w)};
;         ss[mi] += (xa.x * xa.x + xa.y * xa.y) + (xa.z * xa.z + xa.w * xa.w) + (xb.x * xb.x + xb.y * xb.y) + (xb.z * xb.z + xb.w * xb.w);
;         const float u[8] = {xa.x * L.g[0].x, xa.y * L.g[0].y, xa.z * L.g[0].z, xa.w * L.g[0].w, xb.x * L.g[1].x, xb.y * L.g[1].y, xb.z * L.g[1].z, xb.w * L.g[1].w};
;         unsigned hb[8]; float lo[8];
; #pragma unroll
;         for (int j = 0; j < 8; ++j) { hb[j] = f2bf(u[j]); lo[j] = u[j] - __builtin_bit_cast(float, hb[j] << 16); }
;         const u32x4 hw = (u32x4){hb[0] | (hb[1] << 16), hb[2] | (hb[3] << 16), hb[4] | (hb[5] << 16), hb[6] | (hb[7] << 16)};
;         const u32x4 lw = (u32x4){pk2(lo[0], lo[1]), pk2(lo[2], lo[3]), pk2(lo[4], lo[5]), pk2(lo[6], lo[7])};
;         ahi[mi] = __builtin_bit_cast(bf16x8, hw); alo[mi] = __builtin_bit_cast(bf16x8, lw); }
; #pragma unroll
;     for (int n = 0; n < 5; ++n)
; #pragma unroll
;         for (int mi = 0; mi < 2; ++mi) { acc[mi][n] = __builtin_amdgcn_mfma_f32_16x16x32_bf16(ahi[mi], W.wh[n], acc[mi][n], 0, 0, 0);
;             acc[mi][n] = __builtin_amdgcn_mfma_f32_16x16x32_bf16(alo[mi], W.wh[n], acc[mi][n], 0, 0, 0);
;             acc[mi][n] = __builtin_amdgcn_mfma_f32_16x16x32_bf16(ahi[mi], W.wl[n], acc[mi][n], 0, 0, 0); }
; }
; __device__ __forceinline__ void p5_router(Frame& F) {
;     ...
; #pragma unroll 1
;           for (int ks = 0; ks < 32; ks += 2) {
;               rt_load(Lb, h0, h1, gp, (ks + 1) * 32); rt_step(La, bh, bl, acc, ss, ks * 32);
;               if (ks + 2 < 32) rt_load(La, h0, h1, gp, (ks + 2) * 32);
;               rt_step(Lb, bh, bl, acc, ss, (ks + 1) * 32); }
.Lrt_loop_p3:
	v_add_u32_e32 v216, 0x100, v216
	global_load_dwordx4 v[50:53], v216, s[66:67]
	global_load_dwordx4 v[54:57], v216, s[66:67] offset:16
	s_add_i32 m0, s91, s98
	v_add_u32_e32 v208, 0x80, v208
	global_load_lds_dwordx4 v208, s[86:87]
	s_add_i32 m0, s91, s99
	v_add_u32_e32 v209, 0x80, v209
	global_load_lds_dwordx4 v209, s[86:87]
	s_add_i32 m0, s91, s100
	v_add_u32_e32 v210, 0x80, v210
	global_load_lds_dwordx4 v210, s[86:87]
	v_add_u32_e32 v214, s94, v212
	v_add_u32_e32 v215, s94, v213
	ds_read_b128 v[38:41], v215
	ds_read_b128 v[58:61], v214 offset:0
	ds_read_b128 v[62:65], v214 offset:2048
	ds_read_b128 v[66:69], v214 offset:4096
	ds_read_b128 v[70:73], v214 offset:6144
	ds_read_b128 v[74:77], v214 offset:8192
	ds_read_b128 v[100:103], v214 offset:10240
	ds_read_b128 v[104:107], v214 offset:12288
	ds_read_b128 v[108:111], v214 offset:14336
	ds_read_b128 v[112:115], v214 offset:16384
	ds_read_b128 v[116:119], v214 offset:18432
	s_waitcnt vmcnt(8)
	s_waitcnt lgkmcnt(10)
	v_lshlrev_b32_e32 v172, 16, v38
	v_and_b32_e32 v173, 0xffff0000, v38
	v_lshlrev_b32_e32 v174, 16, v39
	v_and_b32_e32 v175, 0xffff0000, v39
	v_lshlrev_b32_e32 v176, 16, v40
	v_and_b32_e32 v177, 0xffff0000, v40
	v_lshlrev_b32_e32 v178, 16, v41
	v_and_b32_e32 v179, 0xffff0000, v41
	v_mul_f32_e32 v180, v42, v172
	v_mul_f32_e32 v181, v43, v173
	v_mul_f32_e32 v182, v44, v174
	v_mul_f32_e32 v183, v45, v175
	v_mul_f32_e32 v184, v46, v176
	v_mul_f32_e32 v185, v47, v177
	v_mul_f32_e32 v186, v48, v178
	v_mul_f32_e32 v187, v49, v179
	v_cvt_pk_bf16_f32 v200, v180, v181
	v_cvt_pk_bf16_f32 v201, v182, v183
	v_cvt_pk_bf16_f32 v202, v184, v185
	v_cvt_pk_bf16_f32 v203, v186, v187
	v_mul_f32_e32 v196, v172, v172
	v_mul_f32_e32 v197, v174, v174
	v_mul_f32_e32 v198, v176, v176
	v_mul_f32_e32 v199, v178, v178
	v_fma_f32 v196, v173, v173, v196
	v_fma_f32 v197, v175, v175, v197
	v_fma_f32 v198, v177, v177, v198
	v_fma_f32 v199, v179, v179, v199
	v_lshlrev_b32_e32 v188, 16, v200
	v_and_b32_e32 v189, 0xffff0000, v200
	v_lshlrev_b32_e32 v190, 16, v201
	v_and_b32_e32 v191, 0xffff0000, v201
	v_lshlrev_b32_e32 v192, 16, v202
	v_and_b32_e32 v193, 0xffff0000, v202
	v_lshlrev_b32_e32 v194, 16, v203
	v_and_b32_e32 v195, 0xffff0000, v203
	v_fma_f32 v180, v42, v172, -v188
	v_fma_f32 v181, v43, v173, -v189
	v_fma_f32 v182, v44, v174, -v190
	v_fma_f32 v183, v45, v175, -v191
	v_fma_f32 v184, v46, v176, -v192
	v_fma_f32 v185, v47, v177, -v193
	v_fma_f32 v186, v48, v178, -v194
	v_fma_f32 v187, v49, v179, -v195
	v_add_f32_e32 v196, v196, v197
	v_add_f32_e32 v196, v196, v198
	v_add_f32_e32 v196, v196, v199
	v_add_f32_e32 v224, v224, v196
	v_cvt_pk_bf16_f32 v204, v180, v181
	v_cvt_pk_bf16_f32 v205, v182, v183
	v_cvt_pk_bf16_f32 v206, v184, v185
	v_cvt_pk_bf16_f32 v207, v186, v187
	s_waitcnt lgkmcnt(0)
	v_mfma_f32_16x16x32_bf16 v[18:21], v[200:203], v[58:61], v[18:21]
	v_mfma_f32_16x16x32_bf16 v[22:25], v[200:203], v[62:65], v[22:25]
	v_mfma_f32_16x16x32_bf16 v[26:29], v[200:203], v[66:69], v[26:29]
	v_mfma_f32_16x16x32_bf16 v[30:33], v[200:203], v[70:73], v[30:33]
	v_mfma_f32_16x16x32_bf16 v[34:37], v[200:203], v[74:77], v[34:37]
	v_mfma_f32_16x16x32_bf16 v[18:21], v[204:207], v[58:61], v[18:21]
	v_mfma_f32_16x16x32_bf16 v[22:25], v[204:207], v[62:65], v[22:25]
	v_mfma_f32_16x16x32_bf16 v[26:29], v[204:207], v[66:69], v[26:29]
	v_mfma_f32_16x16x32_bf16 v[30:33], v[204:207], v[70:73], v[30:33]
	v_mfma_f32_16x16x32_bf16 v[34:37], v[204:207], v[74:77], v[34:37]
	v_mfma_f32_16x16x32_bf16 v[18:21], v[200:203], v[100:103], v[18:21]
	v_mfma_f32_16x16x32_bf16 v[22:25], v[200:203], v[104:107], v[22:25]
	v_mfma_f32_16x16x32_bf16 v[26:29], v[200:203], v[108:111], v[26:29]
	v_mfma_f32_16x16x32_bf16 v[30:33], v[200:203], v[112:115], v[30:33]
	v_mfma_f32_16x16x32_bf16 v[34:37], v[200:203], v[116:119], v[34:37]
	s_waitcnt vmcnt(5)
	s_barrier
	s_mov_b32 s33, s94
	s_mov_b32 s94, s95
	s_mov_b32 s95, s91
	s_mov_b32 s91, s33
	v_add_u32_e32 v216, 0x100, v216
	global_load_dwordx4 v[42:45], v216, s[66:67]
	global_load_dwordx4 v[46:49], v216, s[66:67] offset:16
	s_add_i32 m0, s91, s98
	v_add_u32_e32 v208, 0x80, v208
	global_load_lds_dwordx4 v208, s[86:87]
	s_add_i32 m0, s91, s99
	v_add_u32_e32 v209, 0x80, v209
	global_load_lds_dwordx4 v209, s[86:87]
	s_add_i32 m0, s91, s100
	v_add_u32_e32 v210, 0x80, v210
	global_load_lds_dwordx4 v210, s[86:87]
	v_add_u32_e32 v214, s94, v212
	v_add_u32_e32 v215, s94, v213
	ds_read_b128 v[38:41], v215
	ds_read_b128 v[58:61], v214 offset:0
	ds_read_b128 v[62:65], v214 offset:2048
	ds_read_b128 v[66:69], v214 offset:4096
	ds_read_b128 v[70:73], v214 offset:6144
	ds_read_b128 v[74:77], v214 offset:8192
	ds_read_b128 v[100:103], v214 offset:10240
	ds_read_b128 v[104:107], v214 offset:12288
	ds_read_b128 v[108:111], v214 offset:14336
	ds_read_b128 v[112:115], v214 offset:16384
	ds_read_b128 v[116:119], v214 offset:18432
	s_waitcnt vmcnt(8)
	s_waitcnt lgkmcnt(10)
; __device__ __forceinline__ unsigned f2bf(float f) { unsigned u = __builtin_bit_cast(unsigned, f); return (u + 0x7fffu + ((u >> 16) & 1u)) >> 16; }
; __device__ __forceinline__ void rt_step(const RtLoad& L, const bf16_t* bh, const bf16_t* bl, f32x4 (&acc)[2][5], float (&ss)[2], int ko) {
;     RtW W;
; #pragma unroll
;     for (int n = 0; n < 5; ++n) { W.wh[n] = *(const bf16x8*)(bh + (size_t)n * 16 * D + ko); W.wl[n] = *(const bf16x8*)(bl + (size_t)n * 16 * D + ko); }
;     bf16x8 ahi[2], alo[2];
; #pragma unroll
;     for (int mi = 0; mi < 2; ++mi) { const u32x4 xw = L.x[mi]; const f32x4 xa = (f32x4){bflo(xw.x), bfhi(xw.x), bflo(xw.y), bfhi(xw.y)}, xb = (f32x4){bflo(xw.z), bfhi(xw.z), bflo(xw.w), bfhi(xw.w)};
;         ss[mi] += (xa.x * xa.x + xa.y * xa.y) + (xa.z * xa.z + xa.w * xa.w) + (xb.x * xb.x + xb.y * xb.y) + (xb.z * xb.z + xb.w * xb.w);
;         const float u[8] = {xa.x * L.g[0].x, xa.y * L.g[0].y, xa.z * L.g[0].z, xa.w * L.g[0].w, xb.x * L.g[1].x, xb.y * L.g[1].y, xb.z * L.g[1].z, xb.w * L.g[1].w};
;         unsigned hb[8]; float lo[8];
; #pragma unroll
;         for (int j = 0; j < 8; ++j) { hb[j] = f2bf(u[j]); lo[j] = u[j] - __builtin_bit_cast(float, hb[j] << 16); }
;         const u32x4 hw = (u32x4){hb[0] | (hb[1] << 16), hb[2] | (hb[3] << 16), hb[4] | (hb[5] << 16), hb[6] | (hb[7] << 16)};
;         const u32x4 lw = (u32x4){pk2(lo[0], lo[1]), pk2(lo[2], lo[3]), pk2(lo[4], lo[5]), pk2(lo[6], lo[7])};
;         ahi[mi] = __builtin_bit_cast(bf16x8, hw); alo[mi] = __builtin_bit_cast(bf16x8, lw); }
; #pragma unroll
;     for (int n = 0; n < 5; ++n)
; #pragma unroll
;         for (int mi = 0; mi < 2; ++mi) { acc[mi][n] = __builtin_amdgcn_mfma_f32_16x16x32_bf16(ahi[mi], W.wh[n], acc[mi][n], 0, 0, 0);
;             acc[mi][n] = __builtin_amdgcn_mfma_f32_16x16x32_bf16(alo[mi], W.wh[n], acc[mi][n], 0, 0, 0);
;             acc[mi][n] = __builtin_amdgcn_mfma_f32_16x16x32_bf16(ahi[mi], W.wl[n], acc[mi][n], 0, 0, 0); }
; }
; __device__ __forceinline__ void p5_router(Frame& F) {
;     ...
; #pragma unroll 1
;           for (int ks = 0; ks < 32; ks += 2) {
;               rt_load(Lb, h0, h1, gp, (ks + 1) * 32); rt_step(La, bh, bl, acc, ss, ks * 32);
;               if (ks + 2 < 32) rt_load(La, h0, h1, gp, (ks + 2) * 32);
;               rt_step(Lb, bh, bl, acc, ss, (ks + 1) * 32); }
	v_lshlrev_b32_e32 v172, 16, v38
	v_and_b32_e32 v173, 0xffff0000, v38
	v_lshlrev_b32_e32 v174, 16, v39
	v_and_b32_e32 v175, 0xffff0000, v39
	v_lshlrev_b32_e32 v176, 16, v40
	v_and_b32_e32 v177, 0xffff0000, v40
	v_lshlrev_b32_e32 v178, 16, v41
	v_and_b32_e32 v179, 0xffff0000, v41
	v_mul_f32_e32 v180, v50, v172
	v_mul_f32_e32 v181, v51, v173
	v_mul_f32_e32 v182, v52, v174
	v_mul_f32_e32 v183, v53, v175
	v_mul_f32_e32 v184, v54, v176
	v_mul_f32_e32 v185, v55, v177
	v_mul_f32_e32 v186, v56, v178
	v_mul_f32_e32 v187, v57, v179
	v_cvt_pk_bf16_f32 v200, v180, v181
	v_cvt_pk_bf16_f32 v201, v182, v183
	v_cvt_pk_bf16_f32 v202, v184, v185
	v_cvt_pk_bf16_f32 v203, v186, v187
	v_mul_f32_e32 v196, v172, v172
	v_mul_f32_e32 v197, v174, v174
	v_mul_f32_e32 v198, v176, v176
	v_mul_f32_e32 v199, v178, v178
	v_fma_f32 v196, v173, v173, v196
	v_fma_f32 v197, v175, v175, v197
	v_fma_f32 v198, v177, v177, v198
	v_fma_f32 v199, v179, v179, v199
	v_lshlrev_b32_e32 v188, 16, v200
	v_and_b32_e32 v189, 0xffff0000, v200
	v_lshlrev_b32_e32 v190, 16, v201
	v_and_b32_e32 v191, 0xffff0000, v201
	v_lshlrev_b32_e32 v192, 16, v202
	v_and_b32_e32 v193, 0xffff0000, v202
	v_lshlrev_b32_e32 v194, 16, v203
	v_and_b32_e32 v195, 0xffff0000, v203
	v_fma_f32 v180, v50, v172, -v188
	v_fma_f32 v181, v51, v173, -v189
	v_fma_f32 v182, v52, v174, -v190
	v_fma_f32 v183, v53, v175, -v191
	v_fma_f32 v184, v54, v176, -v192
	v_fma_f32 v185, v55, v177, -v193
	v_fma_f32 v186, v56, v178, -v194
	v_fma_f32 v187, v57, v179, -v195
	v_add_f32_e32 v196, v196, v197
	v_add_f32_e32 v196, v196, v198
	v_add_f32_e32 v196, v196, v199
	v_add_f32_e32 v224, v224, v196
	v_cvt_pk_bf16_f32 v204, v180, v181
	v_cvt_pk_bf16_f32 v205, v182, v183
	v_cvt_pk_bf16_f32 v206, v184, v185
	v_cvt_pk_bf16_f32 v207, v186, v187
	s_waitcnt lgkmcnt(0)
	v_mfma_f32_16x16x32_bf16 v[18:21], v[200:203], v[58:61], v[18:21]
	v_mfma_f32_16x16x32_bf16 v[22:25], v[200:203], v[62:65], v[22:25]
	v_mfma_f32_16x16x32_bf16 v[26:29], v[200:203], v[66:69], v[26:29]
	v_mfma_f32_16x16x32_bf16 v[30:33], v[200:203], v[70:73], v[30:33]
	v_mfma_f32_16x16x32_bf16 v[34:37], v[200:203], v[74:77], v[34:37]
	v_mfma_f32_16x16x32_bf16 v[18:21], v[204:207], v[58:61], v[18:21]
	v_mfma_f32_16x16x32_bf16 v[22:25], v[204:207], v[62:65], v[22:25]
	v_mfma_f32_16x16x32_bf16 v[26:29], v[204:207], v[66:69], v[26:29]
	v_mfma_f32_16x16x32_bf16 v[30:33], v[204:207], v[70:73], v[30:33]
	v_mfma_f32_16x16x32_bf16 v[34:37], v[204:207], v[74:77], v[34:37]
	v_mfma_f32_16x16x32_bf16 v[18:21], v[200:203], v[100:103], v[18:21]
	v_mfma_f32_16x16x32_bf16 v[22:25], v[200:203], v[104:107], v[22:25]
	v_mfma_f32_16x16x32_bf16 v[26:29], v[200:203], v[108:111], v[26:29]
	v_mfma_f32_16x16x32_bf16 v[30:33], v[200:203], v[112:115], v[30:33]
	v_mfma_f32_16x16x32_bf16 v[34:37], v[200:203], v[116:119], v[34:37]
	s_waitcnt vmcnt(5)
	s_barrier
	s_mov_b32 s33, s94
	s_mov_b32 s94, s95
	s_mov_b32 s95, s91
	s_mov_b32 s91, s33
	s_sub_u32 s85, s85, 1
	s_cmp_lg_u32 s85, 0
	s_cbranch_scc1 .Lrt_loop_p3
	v_add_u32_e32 v216, 0x100, v216
	global_load_dwordx4 v[50:53], v216, s[66:67]
	global_load_dwordx4 v[54:57], v216, s[66:67] offset:16
	v_add_u32_e32 v214, s94, v212
	v_add_u32_e32 v215, s94, v213
	ds_read_b128 v[38:41], v215
	ds_read_b128 v[58:61], v214 offset:0
	ds_read_b128 v[62:65], v214 offset:2048
	ds_read_b128 v[66:69], v214 offset:4096
	ds_read_b128 v[70:73], v214 offset:6144
	ds_read_b128 v[74:77], v214 offset:8192
	ds_read_b128 v[100:103], v214 offset:10240
	ds_read_b128 v[104:107], v214 offset:12288
	ds_read_b128 v[108:111], v214 offset:14336
	ds_read_b128 v[112:115], v214 offset:16384
	ds_read_b128 v[116:119], v214 offset:18432
	s_waitcnt vmcnt(5)
	s_waitcnt lgkmcnt(10)
	v_lshlrev_b32_e32 v172, 16, v38
	v_and_b32_e32 v173, 0xffff0000, v38
	v_lshlrev_b32_e32 v174, 16, v39
	v_and_b32_e32 v175, 0xffff0000, v39
	v_lshlrev_b32_e32 v176, 16, v40
	v_and_b32_e32 v177, 0xffff0000, v40
	v_lshlrev_b32_e32 v178, 16, v41
	v_and_b32_e32 v179, 0xffff0000, v41
	v_mul_f32_e32 v180, v42, v172
	v_mul_f32_e32 v181, v43, v173
	v_mul_f32_e32 v182, v44, v174
	v_mul_f32_e32 v183, v45, v175
	v_mul_f32_e32 v184, v46, v176
	v_mul_f32_e32 v185, v47, v177
	v_mul_f32_e32 v186, v48, v178
	v_mul_f32_e32 v187, v49, v179
	v_cvt_pk_bf16_f32 v200, v180, v181
	v_cvt_pk_bf16_f32 v201, v182, v183
	v_cvt_pk_bf16_f32 v202, v184, v185
	v_cvt_pk_bf16_f32 v203, v186, v187
	v_mul_f32_e32 v196, v172, v172
	v_mul_f32_e32 v197, v174, v174
	v_mul_f32_e32 v198, v176, v176
	v_mul_f32_e32 v199, v178, v178
	v_fma_f32 v196, v173, v173, v196
	v_fma_f32 v197, v175, v175, v197
	v_fma_f32 v198, v177, v177, v198
	v_fma_f32 v199, v179, v179, v199
	v_lshlrev_b32_e32 v188, 16, v200
	v_and_b32_e32 v189, 0xffff0000, v200
	v_lshlrev_b32_e32 v190, 16, v201
	v_and_b32_e32 v191, 0xffff0000, v201
	v_lshlrev_b32_e32 v192, 16, v202
	v_and_b32_e32 v193, 0xffff0000, v202
	v_lshlrev_b32_e32 v194, 16, v203
	v_and_b32_e32 v195, 0xffff0000, v203
	v_fma_f32 v180, v42, v172, -v188
	v_fma_f32 v181, v43, v173, -v189
	v_fma_f32 v182, v44, v174, -v190
	v_fma_f32 v183, v45, v175, -v191
	v_fma_f32 v184, v46, v176, -v192
	v_fma_f32 v185, v47, v177, -v193
	v_fma_f32 v186, v48, v178, -v194
	v_fma_f32 v187, v49, v179, -v195
	v_add_f32_e32 v196, v196, v197
	v_add_f32_e32 v196, v196, v198
	v_add_f32_e32 v196, v196, v199
	v_add_f32_e32 v224, v224, v196
	v_cvt_pk_bf16_f32 v204, v180, v181
	v_cvt_pk_bf16_f32 v205, v182, v183
	v_cvt_pk_bf16_f32 v206, v184, v185
	v_cvt_pk_bf16_f32 v207, v186, v187
	s_waitcnt lgkmcnt(0)
	v_mfma_f32_16x16x32_bf16 v[18:21], v[200:203], v[58:61], v[18:21]
	v_mfma_f32_16x16x32_bf16 v[22:25], v[200:203], v[62:65], v[22:25]
	v_mfma_f32_16x16x32_bf16 v[26:29], v[200:203], v[66:69], v[26:29]
	v_mfma_f32_16x16x32_bf16 v[30:33], v[200:203], v[70:73], v[30:33]
	v_mfma_f32_16x16x32_bf16 v[34:37], v[200:203], v[74:77], v[34:37]
	v_mfma_f32_16x16x32_bf16 v[18:21], v[204:207], v[58:61], v[18:21]
	v_mfma_f32_16x16x32_bf16 v[22:25], v[204:207], v[62:65], v[22:25]
	v_mfma_f32_16x16x32_bf16 v[26:29], v[204:207], v[66:69], v[26:29]
	v_mfma_f32_16x16x32_bf16 v[30:33], v[204:207], v[70:73], v[30:33]
	v_mfma_f32_16x16x32_bf16 v[34:37], v[204:207], v[74:77], v[34:37]
	v_mfma_f32_16x16x32_bf16 v[18:21], v[200:203], v[100:103], v[18:21]
	v_mfma_f32_16x16x32_bf16 v[22:25], v[200:203], v[104:107], v[22:25]
	v_mfma_f32_16x16x32_bf16 v[26:29], v[200:203], v[108:111], v[26:29]
	v_mfma_f32_16x16x32_bf16 v[30:33], v[200:203], v[112:115], v[30:33]
	v_mfma_f32_16x16x32_bf16 v[34:37], v[200:203], v[116:119], v[34:37]
	s_waitcnt vmcnt(2)
	s_barrier
; __device__ __forceinline__ void p5_router(Frame& F) {
;     ...
;           for (int ks = 0; ks < 32; ks += 2) {
;               rt_load(Lb, h0, h1, gp, (ks + 1) * 32); rt_step(La, bh, bl, acc, ss, ks * 32);
;               if (ks + 2 < 32) rt_load(La, h0, h1, gp, (ks + 2) * 32);
;               rt_step(Lb, bh, bl, acc, ss, (ks + 1) * 32); }
; #pragma unroll
;           for (int mi = 0; mi < 2; ++mi) { float s = ss[mi]; s += __shfl_xor(s, 16); s += __shfl_xor(s, 32); if (fq == 0) ssp[kq * 64 + 32 * tg + 16 * mi + fr] = s;
; #pragma unroll
;               for (int n = 0; n < 5; ++n)
; #pragma unroll
;                   for (int i = 0; i < 4; ++i) part[(kq * 64 + 32 * tg + 16 * mi + 4 * fq + i) * 80 + 16 * n + fr] = acc[mi][n][i]; } }
;         __syncthreads();
;         if (F.tid < 64) { const float s = (ssp[F.tid] + ssp[64 + F.tid]) + (ssp[128 + F.tid] + ssp[192 + F.tid]); const float r = 1.0f / sqrtf(s * (1.f / D) + RMS_EPS); rs[F.tid] = r; }
;         __syncthreads();
	s_mov_b32 s33, s94
	s_mov_b32 s94, s95
	s_mov_b32 s95, s91
	s_mov_b32 s91, s33
	v_add_u32_e32 v214, s94, v212
	v_add_u32_e32 v215, s94, v213
	ds_read_b128 v[38:41], v215
	ds_read_b128 v[58:61], v214 offset:0
	ds_read_b128 v[62:65], v214 offset:2048
	ds_read_b128 v[66:69], v214 offset:4096
	ds_read_b128 v[70:73], v214 offset:6144
	ds_read_b128 v[74:77], v214 offset:8192
	ds_read_b128 v[100:103], v214 offset:10240
	ds_read_b128 v[104:107], v214 offset:12288
	ds_read_b128 v[108:111], v214 offset:14336
	ds_read_b128 v[112:115], v214 offset:16384
	ds_read_b128 v[116:119], v214 offset:18432
	s_waitcnt vmcnt(0)
	s_waitcnt lgkmcnt(10)
	v_lshlrev_b32_e32 v172, 16, v38
	v_and_b32_e32 v173, 0xffff0000, v38
	v_lshlrev_b32_e32 v174, 16, v39
	v_and_b32_e32 v175, 0xffff0000, v39
	v_lshlrev_b32_e32 v176, 16, v40
	v_and_b32_e32 v177, 0xffff0000, v40
	v_lshlrev_b32_e32 v178, 16, v41
	v_and_b32_e32 v179, 0xffff0000, v41
	v_mul_f32_e32 v180, v50, v172
	v_mul_f32_e32 v181, v51, v173
	v_mul_f32_e32 v182, v52, v174
	v_mul_f32_e32 v183, v53, v175
	v_mul_f32_e32 v184, v54, v176
	v_mul_f32_e32 v185, v55, v177
	v_mul_f32_e32 v186, v56, v178
	v_mul_f32_e32 v187, v57, v179
	v_cvt_pk_bf16_f32 v200, v180, v181
	v_cvt_pk_bf16_f32 v201, v182, v183
	v_cvt_pk_bf16_f32 v202, v184, v185
	v_cvt_pk_bf16_f32 v203, v186, v187
	v_mul_f32_e32 v196, v172, v172
	v_mul_f32_e32 v197, v174, v174
	v_mul_f32_e32 v198, v176, v176
	v_mul_f32_e32 v199, v178, v178
	v_fma_f32 v196, v173, v173, v196
	v_fma_f32 v197, v175, v175, v197
	v_fma_f32 v198, v177, v177, v198
	v_fma_f32 v199, v179, v179, v199
	v_lshlrev_b32_e32 v188, 16, v200
	v_and_b32_e32 v189, 0xffff0000, v200
	v_lshlrev_b32_e32 v190, 16, v201
	v_and_b32_e32 v191, 0xffff0000, v201
	v_lshlrev_b32_e32 v192, 16, v202
	v_and_b32_e32 v193, 0xffff0000, v202
	v_lshlrev_b32_e32 v194, 16, v203
	v_and_b32_e32 v195, 0xffff0000, v203
	v_fma_f32 v180, v50, v172, -v188
	v_fma_f32 v181, v51, v173, -v189
	v_fma_f32 v182, v52, v174, -v190
	v_fma_f32 v183, v53, v175, -v191
	v_fma_f32 v184, v54, v176, -v192
	v_fma_f32 v185, v55, v177, -v193
	v_fma_f32 v186, v56, v178, -v194
	v_fma_f32 v187, v57, v179, -v195
	v_add_f32_e32 v196, v196, v197
	v_add_f32_e32 v196, v196, v198
	v_add_f32_e32 v196, v196, v199
	v_add_f32_e32 v224, v224, v196
	v_cvt_pk_bf16_f32 v204, v180, v181
	v_cvt_pk_bf16_f32 v205, v182, v183
	v_cvt_pk_bf16_f32 v206, v184, v185
	v_cvt_pk_bf16_f32 v207, v186, v187
	s_waitcnt lgkmcnt(0)
	v_mfma_f32_16x16x32_bf16 v[18:21], v[200:203], v[58:61], v[18:21]
	v_mfma_f32_16x16x32_bf16 v[22:25], v[200:203], v[62:65], v[22:25]
	v_mfma_f32_16x16x32_bf16 v[26:29], v[200:203], v[66:69], v[26:29]
	v_mfma_f32_16x16x32_bf16 v[30:33], v[200:203], v[70:73], v[30:33]
	v_mfma_f32_16x16x32_bf16 v[34:37], v[200:203], v[74:77], v[34:37]
	v_mfma_f32_16x16x32_bf16 v[18:21], v[204:207], v[58:61], v[18:21]
	v_mfma_f32_16x16x32_bf16 v[22:25], v[204:207], v[62:65], v[22:25]
	v_mfma_f32_16x16x32_bf16 v[26:29], v[204:207], v[66:69], v[26:29]
	v_mfma_f32_16x16x32_bf16 v[30:33], v[204:207], v[70:73], v[30:33]
	v_mfma_f32_16x16x32_bf16 v[34:37], v[204:207], v[74:77], v[34:37]
	v_mfma_f32_16x16x32_bf16 v[18:21], v[200:203], v[100:103], v[18:21]
	v_mfma_f32_16x16x32_bf16 v[22:25], v[200:203], v[104:107], v[22:25]
	v_mfma_f32_16x16x32_bf16 v[26:29], v[200:203], v[108:111], v[26:29]
	v_mfma_f32_16x16x32_bf16 v[30:33], v[200:203], v[112:115], v[30:33]
	v_mfma_f32_16x16x32_bf16 v[34:37], v[200:203], v[116:119], v[34:37]
	s_barrier
	s_mov_b32 s33, s94
	s_mov_b32 s94, s95
	s_mov_b32 s95, s91
	s_mov_b32 s91, s33
.Lrt_out:
	s_lshl_b32 s24, s89, 6
	s_lshl_b32 s33, s88, 4
	s_add_i32 s24, s24, s33
	s_mul_i32 s33, s24, 320
	v_mul_u32_u24_e32 v217, 0x500, v171
	v_lshl_add_u32 v217, v170, 2, v217
	v_add_u32_e32 v217, s33, v217
	ds_write_b32 v217, v18 offset:0
	ds_write_b32 v217, v19 offset:320
	ds_write_b32 v217, v20 offset:640
	ds_write_b32 v217, v21 offset:960
	ds_write_b32 v217, v22 offset:64
	ds_write_b32 v217, v23 offset:384
	ds_write_b32 v217, v24 offset:704
	ds_write_b32 v217, v25 offset:1024
	ds_write_b32 v217, v26 offset:128
	ds_write_b32 v217, v27 offset:448
	ds_write_b32 v217, v28 offset:768
	ds_write_b32 v217, v29 offset:1088
	ds_write_b32 v217, v30 offset:192
	ds_write_b32 v217, v31 offset:512
	ds_write_b32 v217, v32 offset:832
	ds_write_b32 v217, v33 offset:1152
	ds_write_b32 v217, v34 offset:256
	ds_write_b32 v217, v35 offset:576
	ds_write_b32 v217, v36 offset:896
	ds_write_b32 v217, v37 offset:1216
	v_mov_b32_e32 v218, 0
	v_mov_b32_e32 v219, 0
	v_mov_b32_e32 v220, 0
	v_mov_b32_e32 v221, 0
	v_lshlrev_b32_e32 v222, 4, v0
	v_add_u32_e32 v222, 0xa000, v222
	ds_write_b128 v222, v[218:221] offset:0
	ds_write_b128 v222, v[218:221] offset:8192
	ds_write_b128 v222, v[218:221] offset:16384
	ds_write_b128 v222, v[218:221] offset:24576
	ds_write_b128 v222, v[218:221] offset:32768
	ds_bpermute_b32 v223, v144, v224
	s_waitcnt lgkmcnt(0)
	v_add_f32_e32 v223, v224, v223
	ds_bpermute_b32 v222, v145, v223
	s_lshl_b32 s24, s24, 2
	s_add_i32 s24, s24, 0x19000
	v_lshl_add_u32 v217, v170, 2, s24
	s_waitcnt lgkmcnt(0)
	v_add_f32_e32 v223, v223, v222
	s_and_saveexec_b64 s[98:99], s[6:7]
	ds_write_b32 v217, v223
	s_or_b64 exec, exec, s[98:99]
	v_cmp_gt_u32_e32 vcc, 0x80, v0
	v_lshlrev_b32_e32 v222, 2, v0
	v_add_u32_e32 v222, 0x19200, v222
	s_and_saveexec_b64 s[98:99], vcc
	ds_write_b32 v222, v218
	s_or_b64 exec, exec, s[98:99]
	s_waitcnt lgkmcnt(0)
	s_barrier
	s_and_saveexec_b64 s[8:9], s[4:5]
	s_cbranch_execz .LBB0_616
	ds_read2st64_b32 v[2:3], v147 offset1:1
	ds_read2st64_b32 v[4:5], v147 offset0:2 offset1:3
	s_waitcnt lgkmcnt(1)
	v_mov_b32_e32 v6, v2
	s_waitcnt lgkmcnt(0)
	v_mov_b32_e32 v7, v4
	v_mov_b32_e32 v4, v3
	v_pk_add_f32 v[2:3], v[6:7], v[4:5]
	s_nop 0
	v_add_f32_e32 v2, v2, v3
	v_fmamk_f32 v2, v2, 0x39800000, v151
	v_mul_f32_e32 v3, 0x4f800000, v2
	v_cmp_gt_f32_e32 vcc, s57, v2
	s_nop 1
	v_cndmask_b32_e32 v2, v2, v3, vcc
	v_sqrt_f32_e32 v3, v2
	s_nop 0
	v_add_u32_e32 v4, -1, v3
	v_add_u32_e32 v5, 1, v3
	v_fma_f32 v6, -v4, v3, v2
	v_fma_f32 v7, -v5, v3, v2
	v_cmp_ge_f32_e64 s[0:1], 0, v6
	s_nop 1
	v_cndmask_b32_e64 v3, v3, v4, s[0:1]
	v_cmp_lt_f32_e64 s[0:1], 0, v7
	s_nop 1
	v_cndmask_b32_e64 v3, v3, v5, s[0:1]
	v_mul_f32_e32 v4, 0x37800000, v3
	v_cndmask_b32_e32 v3, v3, v4, vcc
	v_cmp_class_f32_e32 vcc, v2, v152
	s_nop 1
	v_cndmask_b32_e32 v2, v3, v2, vcc
	v_div_scale_f32 v3, s[0:1], v2, v2, 1.0
	v_rcp_f32_e32 v4, v3
	s_nop 0
	v_fma_f32 v5, -v3, v4, 1.0
	v_fmac_f32_e32 v4, v5, v4
	v_div_scale_f32 v5, vcc, 1.0, v2, 1.0
	v_mul_f32_e32 v6, v5, v4
	v_fma_f32 v7, -v3, v6, v5
	v_fmac_f32_e32 v6, v7, v4
	v_fma_f32 v3, -v3, v6, v5
	v_div_fmas_f32 v3, v3, v4, v6
	v_div_fixup_f32 v2, v3, v2, 1.0
	ds_write_b32 v148, v2

; __global__ void __launch_bounds__(NTHREADS, 2) hymba_fwd(Args args) {
	.amdhsa_kernel _Z9hymba_fwd4Args
		.amdhsa_group_segment_fixed_size 19520
		.amdhsa_private_segment_fixed_size 0
		.amdhsa_kernarg_size 424
		.amdhsa_user_sgpr_count 2
		.amdhsa_user_sgpr_dispatch_ptr 0
		.amdhsa_user_sgpr_queue_ptr 0
		.amdhsa_user_sgpr_kernarg_segment_ptr 1
		.amdhsa_user_sgpr_dispatch_id 0
		.amdhsa_user_sgpr_kernarg_preload_length 0
		.amdhsa_user_sgpr_kernarg_preload_offset 0
		.amdhsa_user_sgpr_private_segment_size 0
		.amdhsa_uses_dynamic_stack 0
		.amdhsa_enable_private_segment 0
		.amdhsa_system_sgpr_workgroup_id_x 1
		.amdhsa_system_sgpr_workgroup_id_y 0
		.amdhsa_system_sgpr_workgroup_id_z 0
		.amdhsa_system_sgpr_workgroup_info 0
		.amdhsa_system_vgpr_workitem_id 0
		.amdhsa_next_free_vgpr 255
		.amdhsa_next_free_sgpr 102
		.amdhsa_accum_offset 256
		.amdhsa_reserve_vcc 1
		.amdhsa_float_round_mode_32 0
		.amdhsa_float_round_mode_16_64 0
		.amdhsa_float_denorm_mode_32 3
		.amdhsa_float_denorm_mode_16_64 3
		.amdhsa_dx10_clamp 1
		.amdhsa_ieee_mode 1
		.amdhsa_fp16_overflow 0
		.amdhsa_tg_split 0
		.amdhsa_exception_fp_ieee_invalid_op 0
		.amdhsa_exception_fp_denorm_src 0
		.amdhsa_exception_fp_ieee_div_zero 0
		.amdhsa_exception_fp_ieee_overflow 0
		.amdhsa_exception_fp_ieee_underflow 0
		.amdhsa_exception_fp_ieee_inexact 0
		.amdhsa_exception_int_div_zero 0
	.end_amdhsa_kernel

; __global__ void __launch_bounds__(NTHREADS, 2) hymba_fwd(Args args) {
amdhsa.kernels:
  - .agpr_count:     0
    .args:
      - .offset:         0
        .size:           168
        .value_kind:     by_value
      - .offset:         168
        .size:           4
        .value_kind:     hidden_block_count_x
      - .offset:         172
        .size:           4
        .value_kind:     hidden_block_count_y
      - .offset:         176
        .size:           4
        .value_kind:     hidden_block_count_z
      - .offset:         180
        .size:           2
        .value_kind:     hidden_group_size_x
      - .offset:         182
        .size:           2
        .value_kind:     hidden_group_size_y
      - .offset:         184
        .size:           2
        .value_kind:     hidden_group_size_z
      - .offset:         186
        .size:           2
        .value_kind:     hidden_remainder_x
      - .offset:         188
        .size:           2
        .value_kind:     hidden_remainder_y
      - .offset:         190
        .size:           2
        .value_kind:     hidden_remainder_z
      - .offset:         208
        .size:           8
        .value_kind:     hidden_global_offset_x
      - .offset:         216
        .size:           8
        .value_kind:     hidden_global_offset_y
      - .offset:         224
        .size:           8
        .value_kind:     hidden_global_offset_z
      - .offset:         232
        .size:           2
        .value_kind:     hidden_grid_dims
      - .offset:         288
        .size:           4
        .value_kind:     hidden_dynamic_lds_size
    .group_segment_fixed_size: 19520
    .kernarg_segment_align: 8
    .kernarg_segment_size: 424
    .language:       OpenCL C
    .language_version:
      - 2
      - 0
    .max_flat_workgroup_size: 512
    .name:           _Z9hymba_fwd4Args
    .private_segment_fixed_size: 0
    .sgpr_count:     108
    .sgpr_spill_count: 62
    .symbol:         _Z9hymba_fwd4Args.kd
    .uniform_work_group_size: 1
    .uses_dynamic_stack: false
    .vgpr_count:     255
    .vgpr_spill_count: 0
    .wavefront_size: 64
